# FFN-up epilogue: dead zero-initialisations feeding full-mask row_ror DPP moves replaced by s_nop (same wait states, no VALU slot)
# speedup vs baseline: 1.0054x; 1.0054x over previous
.LBB0_1669:
	s_or_b64 exec, exec, s[34:35]
	v_or_b32_e32 v103, 0xffffffe0, v102
	v_add_u32_e32 v102, s60, v103
	v_lshl_add_u32 v195, v144, 2, s75
	s_and_b64 s[40:41], s[18:19], vcc
	v_mov_b32_e32 v108, 0
	v_lshl_add_u32 v171, v102, 9, v195
	v_mov_b32_e32 v144, 0
	v_mov_b32_e32 v145, 0
	v_mov_b32_e32 v146, 0
	v_mov_b32_e32 v147, 0
	s_and_saveexec_b64 s[34:35], s[40:41]
	ds_read_b128 v[144:147], v171
	s_or_b64 exec, exec, s[34:35]
	v_mov_b32_e32 v109, 0
	v_mov_b32_e32 v110, 0
	v_mov_b32_e32 v111, 0
	s_and_saveexec_b64 s[34:35], s[40:41]
	ds_read_b128 v[108:111], v171 offset:512
	s_or_b64 exec, exec, s[34:35]
	s_waitcnt lgkmcnt(0)
	v_pk_mul_f32 v[222:223], v[128:129], v[140:141]
	v_pk_mul_f32 v[224:225], v[128:129], v[136:137]
	v_pk_mul_f32 v[226:227], v[128:129], v[132:133]
	v_pk_mul_f32 v[124:125], v[112:113], v[124:125]
	v_pk_mul_f32 v[128:129], v[114:115], v[122:123]
	v_pk_mul_f32 v[120:121], v[112:113], v[120:121]
	v_pk_mul_f32 v[122:123], v[112:113], v[116:117]
	v_cvt_f32_i32_e32 v113, v22
	v_cvt_f32_i32_e32 v112, v46
	s_nop 0
	s_nop 0
	v_pk_mul_f32 v[142:143], v[130:131], v[142:143]
	v_pk_mul_f32 v[220:221], v[130:131], v[138:139]
	v_pk_mul_f32 v[140:141], v[130:131], v[134:135]
	v_pk_mul_f32 v[130:131], v[114:115], v[118:119]
	s_nop 0
	v_mov_b32_dpp v116, v144 row_ror:2 row_mask:0xf bank_mask:0xf
	s_nop 0
	v_mov_b32_dpp v117, v108 row_ror:2 row_mask:0xf bank_mask:0xf
	s_waitcnt vmcnt(0)
	v_pk_mul_f32 v[236:237], v[172:173], v[112:113] op_sel_hi:[0,1]
	v_pk_mul_f32 v[126:127], v[114:115], v[126:127]
	v_mov_b32_dpp v118, v144 row_ror:1 row_mask:0xf bank_mask:0xf
	s_nop 0
	s_nop 0
	s_nop 0
	s_nop 0
	v_mov_b32_dpp v119, v108 row_ror:1 row_mask:0xf bank_mask:0xf
	v_mov_b32_dpp v116, v236 row_shr:2 row_mask:0xf bank_mask:0xf
	v_mov_b32_dpp v117, v237 row_shr:2 row_mask:0xf bank_mask:0xf
	v_mov_b32_e32 v112, v124
	v_mov_b32_e32 v113, v222
	v_mov_b32_e32 v114, v104
	v_mov_b32_e32 v115, v98
	v_mov_b32_dpp v136, v146 row_ror:1 row_mask:0xf bank_mask:0xf
	v_mov_b32_dpp v144, v146 row_ror:2 row_mask:0xf bank_mask:0xf
	v_mov_b32_dpp v232, v147 row_ror:1 row_mask:0xf bank_mask:0xf
	v_mov_b32_dpp v234, v147 row_ror:2 row_mask:0xf bank_mask:0xf
	v_mov_b32_dpp v118, v236 row_shr:1 row_mask:0xf bank_mask:0xf
	v_mov_b32_dpp v119, v237 row_shr:1 row_mask:0xf bank_mask:0xf
	v_pk_fma_f32 v[146:147], v[112:113], v[116:117], v[114:115]
	v_mov_b32_e32 v116, v120
	v_mov_b32_e32 v117, v224
	v_pk_fma_f32 v[146:147], v[116:117], v[118:119], v[146:147]
	v_mov_b32_e32 v118, v122
	v_mov_b32_e32 v119, v226
	v_pk_fma_f32 v[238:239], v[236:237], v[118:119], v[146:147]
	v_cvt_f32_i32_e32 v147, v23
	v_cvt_f32_i32_e32 v146, v47
	s_nop 0
	s_nop 0
	s_nop 0
	v_mov_b32_dpp v134, v145 row_ror:2 row_mask:0xf bank_mask:0xf
	v_mov_b32_dpp v133, v109 row_ror:1 row_mask:0xf bank_mask:0xf
	v_mov_b32_dpp v135, v109 row_ror:2 row_mask:0xf bank_mask:0xf
	v_pk_mul_f32 v[108:109], v[172:173], v[146:147] op_sel_hi:[0,1]
	s_nop 0
	v_mov_b32_e32 v222, v125
	v_mov_b32_dpp v134, v108 row_shr:2 row_mask:0xf bank_mask:0xf
	v_mov_b32_dpp v135, v109 row_shr:2 row_mask:0xf bank_mask:0xf
	v_mov_b32_e32 v98, v105
	v_mov_b32_dpp v132, v145 row_ror:1 row_mask:0xf bank_mask:0xf
	v_pk_fma_f32 v[104:105], v[222:223], v[134:135], v[98:99]
	v_mov_b32_e32 v224, v121
	v_cvt_f32_i32_e32 v121, v24
	v_cvt_f32_i32_e32 v120, v48
	v_cvt_f32_i32_e32 v135, v25
	v_cvt_f32_i32_e32 v134, v49
	v_mov_b32_dpp v132, v108 row_shr:1 row_mask:0xf bank_mask:0xf
	v_mov_b32_dpp v133, v109 row_shr:1 row_mask:0xf bank_mask:0xf
	v_pk_fma_f32 v[104:105], v[224:225], v[132:133], v[104:105]
	v_mov_b32_e32 v226, v123
	v_pk_fma_f32 v[104:105], v[108:109], v[226:227], v[104:105]
	s_nop 0
	s_nop 0
	s_nop 0
	s_nop 0
	v_mov_b32_dpp v137, v110 row_ror:1 row_mask:0xf bank_mask:0xf
	v_mov_b32_dpp v145, v110 row_ror:2 row_mask:0xf bank_mask:0xf
	v_pk_mul_f32 v[132:133], v[172:173], v[120:121] op_sel_hi:[0,1]
	v_mov_b32_e32 v121, v142
	v_mov_b32_dpp v233, v111 row_ror:1 row_mask:0xf bank_mask:0xf
	v_mov_b32_dpp v235, v111 row_ror:2 row_mask:0xf bank_mask:0xf
	v_pk_mul_f32 v[110:111], v[172:173], v[134:135] op_sel_hi:[0,1]
	v_mov_b32_e32 v142, v127
	v_mul_f32_e32 v127, 0xbfb8aa3b, v104
	v_mov_b32_dpp v144, v132 row_shr:2 row_mask:0xf bank_mask:0xf
	v_mov_b32_dpp v145, v133 row_shr:2 row_mask:0xf bank_mask:0xf
	v_mov_b32_e32 v120, v126
	v_mov_b32_e32 v122, v106
	v_mov_b32_e32 v123, v100
	v_mov_b32_dpp v234, v110 row_shr:2 row_mask:0xf bank_mask:0xf
	v_mov_b32_dpp v235, v111 row_shr:2 row_mask:0xf bank_mask:0xf
	v_mov_b32_e32 v100, v107
	v_exp_f32_e32 v127, v127
	v_mov_b32_dpp v136, v132 row_shr:1 row_mask:0xf bank_mask:0xf
	v_mov_b32_dpp v137, v133 row_shr:1 row_mask:0xf bank_mask:0xf
	v_pk_fma_f32 v[124:125], v[120:121], v[144:145], v[122:123]
	v_mov_b32_e32 v144, v128
	v_mov_b32_e32 v145, v220
	v_mov_b32_dpp v232, v110 row_shr:1 row_mask:0xf bank_mask:0xf
	v_mov_b32_dpp v233, v111 row_shr:1 row_mask:0xf bank_mask:0xf
	v_pk_fma_f32 v[106:107], v[142:143], v[234:235], v[100:101]
	v_mov_b32_e32 v220, v129
	v_pk_fma_f32 v[124:125], v[144:145], v[136:137], v[124:125]
	v_mov_b32_e32 v146, v130
	v_mov_b32_e32 v147, v140
	v_pk_fma_f32 v[106:107], v[220:221], v[232:233], v[106:107]
	v_mov_b32_e32 v140, v131
	v_pk_fma_f32 v[124:125], v[132:133], v[146:147], v[124:125]
	v_pk_fma_f32 v[106:107], v[110:111], v[140:141], v[106:107]
	v_add_f32_e32 v127, 1.0, v127
	v_mul_f32_e32 v128, 0xbfb8aa3b, v124
	v_mul_f32_e32 v129, 0xbfb8aa3b, v106
	v_mul_f32_e32 v126, 0xbfb8aa3b, v238
	v_rcp_f32_e32 v127, v127
	v_exp_f32_e32 v128, v128
	v_exp_f32_e32 v129, v129
	v_exp_f32_e32 v126, v126
	v_mul_f32_e32 v104, v104, v127
	v_add_f32_e32 v127, 1.0, v128
	v_add_f32_e32 v128, 1.0, v129
	v_add_f32_e32 v126, 1.0, v126
	v_rcp_f32_e32 v127, v127
	v_rcp_f32_e32 v128, v128
	v_rcp_f32_e32 v126, v126
	v_cvt_f32_i32_e32 v137, v18
	v_cvt_f32_i32_e32 v136, v42
	v_mul_f32_e32 v104, v104, v105
	v_mul_f32_e32 v105, v124, v127
	v_mul_f32_e32 v106, v106, v128
	v_lshl_add_u64 v[138:139], v[156:157], 1, s[8:9]
	v_mul_f32_e32 v126, v238, v126
	v_mul_f32_e32 v105, v105, v125
	v_mul_f32_e32 v106, v106, v107
	v_mul_f32_e32 v126, v126, v239
	v_cvt_pk_bf16_f32 v104, v126, v104
	v_cvt_pk_bf16_f32 v105, v105, v106
	v_mad_u64_u32 v[124:125], s[34:35], v169, s72, v[138:139]
	s_nop 0
	s_nop 0
	global_store_dwordx2 v[124:125], v[104:105], off
	s_nop 0
	v_mov_b32_dpp v106, v236 row_ror:2 row_mask:0xf bank_mask:0xf
	s_nop 0
	v_mov_b32_dpp v107, v237 row_ror:2 row_mask:0xf bank_mask:0xf
	v_pk_mul_f32 v[136:137], v[170:171], v[136:137] op_sel_hi:[0,1]
	v_mov_b32_dpp v104, v236 row_ror:1 row_mask:0xf bank_mask:0xf
	v_mov_b32_dpp v105, v237 row_ror:1 row_mask:0xf bank_mask:0xf
	v_mov_b32_dpp v106, v136 row_shr:2 row_mask:0xf bank_mask:0xf
	v_mov_b32_dpp v107, v137 row_shr:2 row_mask:0xf bank_mask:0xf
	v_mov_b32_dpp v104, v136 row_shr:1 row_mask:0xf bank_mask:0xf
	v_mov_b32_dpp v105, v137 row_shr:1 row_mask:0xf bank_mask:0xf
	v_pk_fma_f32 v[106:107], v[112:113], v[106:107], v[114:115]
	s_nop 0
	v_pk_fma_f32 v[104:105], v[116:117], v[104:105], v[106:107]
	v_cvt_f32_i32_e32 v107, v19
	v_cvt_f32_i32_e32 v106, v43
	s_nop 0
	s_nop 0
	v_mov_b32_dpp v128, v108 row_ror:2 row_mask:0xf bank_mask:0xf
	s_nop 0
	v_mov_b32_dpp v129, v109 row_ror:2 row_mask:0xf bank_mask:0xf
	v_pk_mul_f32 v[106:107], v[170:171], v[106:107] op_sel_hi:[0,1]
	v_mov_b32_dpp v126, v108 row_ror:1 row_mask:0xf bank_mask:0xf
	v_mov_b32_dpp v127, v109 row_ror:1 row_mask:0xf bank_mask:0xf
	v_mov_b32_dpp v128, v106 row_shr:2 row_mask:0xf bank_mask:0xf
	v_mov_b32_dpp v129, v107 row_shr:2 row_mask:0xf bank_mask:0xf
	v_mov_b32_dpp v126, v106 row_shr:1 row_mask:0xf bank_mask:0xf
	v_mov_b32_dpp v127, v107 row_shr:1 row_mask:0xf bank_mask:0xf
	v_pk_fma_f32 v[128:129], v[222:223], v[128:129], v[98:99]
	s_nop 0
	v_pk_fma_f32 v[126:127], v[224:225], v[126:127], v[128:129]
	v_cvt_f32_i32_e32 v129, v20
	v_cvt_f32_i32_e32 v128, v44
	s_nop 0
	s_nop 0
	v_mov_b32_dpp v130, v132 row_ror:2 row_mask:0xf bank_mask:0xf
	s_nop 0
	v_mov_b32_dpp v131, v133 row_ror:2 row_mask:0xf bank_mask:0xf
	v_pk_mul_f32 v[128:129], v[170:171], v[128:129] op_sel_hi:[0,1]
	v_mov_b32_dpp v108, v132 row_ror:1 row_mask:0xf bank_mask:0xf
	v_mov_b32_dpp v109, v133 row_ror:1 row_mask:0xf bank_mask:0xf
	v_mov_b32_dpp v130, v128 row_shr:2 row_mask:0xf bank_mask:0xf
	v_mov_b32_dpp v131, v129 row_shr:2 row_mask:0xf bank_mask:0xf
	v_mov_b32_dpp v108, v128 row_shr:1 row_mask:0xf bank_mask:0xf
	v_mov_b32_dpp v109, v129 row_shr:1 row_mask:0xf bank_mask:0xf
	v_pk_fma_f32 v[130:131], v[120:121], v[130:131], v[122:123]
	s_nop 0
	v_pk_fma_f32 v[108:109], v[144:145], v[108:109], v[130:131]
	v_cvt_f32_i32_e32 v131, v21
	v_cvt_f32_i32_e32 v130, v45
	s_nop 0
	v_pk_fma_f32 v[104:105], v[136:137], v[118:119], v[104:105]
	s_nop 0
	s_nop 0
	v_mov_b32_dpp v132, v110 row_ror:1 row_mask:0xf bank_mask:0xf
	v_mov_b32_dpp v134, v110 row_ror:2 row_mask:0xf bank_mask:0xf
	v_mov_b32_dpp v133, v111 row_ror:1 row_mask:0xf bank_mask:0xf
	v_mov_b32_dpp v135, v111 row_ror:2 row_mask:0xf bank_mask:0xf
	v_pk_mul_f32 v[110:111], v[170:171], v[130:131] op_sel_hi:[0,1]
	v_mul_f32_e32 v130, 0xbfb8aa3b, v104
	v_exp_f32_e32 v207, v130
	v_mov_b32_dpp v134, v110 row_shr:2 row_mask:0xf bank_mask:0xf
	v_mov_b32_dpp v135, v111 row_shr:2 row_mask:0xf bank_mask:0xf
	v_mov_b32_dpp v132, v110 row_shr:1 row_mask:0xf bank_mask:0xf
	v_mov_b32_dpp v133, v111 row_shr:1 row_mask:0xf bank_mask:0xf
	v_pk_fma_f32 v[130:131], v[142:143], v[134:135], v[100:101]
	v_pk_fma_f32 v[126:127], v[106:107], v[226:227], v[126:127]
	v_pk_fma_f32 v[130:131], v[220:221], v[132:133], v[130:131]
	v_add_f32_e32 v132, 1.0, v207
	v_rcp_f32_e32 v132, v132
	v_mul_f32_e32 v133, 0xbfb8aa3b, v126
	v_exp_f32_e32 v133, v133
	v_pk_fma_f32 v[108:109], v[128:129], v[146:147], v[108:109]
	v_mul_f32_e32 v104, v104, v132
	v_pk_fma_f32 v[130:131], v[110:111], v[140:141], v[130:131]
	v_mul_f32_e32 v104, v104, v105
	v_add_f32_e32 v105, 1.0, v133
	v_mul_f32_e32 v132, 0xbfb8aa3b, v108
	v_rcp_f32_e32 v105, v105
	v_exp_f32_e32 v132, v132
	v_mul_f32_e32 v133, 0xbfb8aa3b, v130
	v_exp_f32_e32 v133, v133
	v_mul_f32_e32 v105, v126, v105
	v_add_f32_e32 v126, 1.0, v132
	v_rcp_f32_e32 v126, v126
	v_add_f32_e32 v132, 1.0, v133
	v_rcp_f32_e32 v132, v132
	v_cvt_f32_i32_e32 v233, v14
	v_mul_f32_e32 v108, v108, v126
	v_cvt_f32_i32_e32 v232, v38
	v_mul_f32_e32 v105, v105, v127
	v_mul_f32_e32 v108, v108, v109
	v_mul_f32_e32 v109, v130, v132
	v_mul_f32_e32 v109, v109, v131
	v_cvt_pk_bf16_f32 v104, v104, v105
	v_cvt_pk_bf16_f32 v105, v108, v109
	v_add_u32_e32 v108, 16, v169
	v_mad_u64_u32 v[126:127], s[34:35], v108, s72, v[138:139]
	s_nop 0
	s_nop 0
	global_store_dwordx2 v[126:127], v[104:105], off
	s_nop 0
	v_mov_b32_dpp v108, v136 row_ror:2 row_mask:0xf bank_mask:0xf
	s_nop 0
	v_mov_b32_dpp v109, v137 row_ror:2 row_mask:0xf bank_mask:0xf
	v_pk_mul_f32 v[232:233], v[168:169], v[232:233] op_sel_hi:[0,1]
	v_mov_b32_dpp v104, v136 row_ror:1 row_mask:0xf bank_mask:0xf
	v_mov_b32_dpp v105, v137 row_ror:1 row_mask:0xf bank_mask:0xf
	v_mov_b32_dpp v108, v232 row_shr:2 row_mask:0xf bank_mask:0xf
	v_mov_b32_dpp v109, v233 row_shr:2 row_mask:0xf bank_mask:0xf
	v_mov_b32_dpp v104, v232 row_shr:1 row_mask:0xf bank_mask:0xf
	v_mov_b32_dpp v105, v233 row_shr:1 row_mask:0xf bank_mask:0xf
	v_pk_fma_f32 v[108:109], v[112:113], v[108:109], v[114:115]
	s_nop 0
	v_pk_fma_f32 v[104:105], v[116:117], v[104:105], v[108:109]
	v_cvt_f32_i32_e32 v109, v15
	v_cvt_f32_i32_e32 v108, v39
	s_nop 0
	s_nop 0
	v_mov_b32_dpp v132, v106 row_ror:2 row_mask:0xf bank_mask:0xf
	s_nop 0
	v_mov_b32_dpp v133, v107 row_ror:2 row_mask:0xf bank_mask:0xf
	v_pk_mul_f32 v[108:109], v[168:169], v[108:109] op_sel_hi:[0,1]
	v_mov_b32_dpp v130, v106 row_ror:1 row_mask:0xf bank_mask:0xf
	v_mov_b32_dpp v131, v107 row_ror:1 row_mask:0xf bank_mask:0xf
	v_mov_b32_dpp v132, v108 row_shr:2 row_mask:0xf bank_mask:0xf
	v_mov_b32_dpp v133, v109 row_shr:2 row_mask:0xf bank_mask:0xf
	v_mov_b32_dpp v130, v108 row_shr:1 row_mask:0xf bank_mask:0xf
	v_mov_b32_dpp v131, v109 row_shr:1 row_mask:0xf bank_mask:0xf
	v_pk_fma_f32 v[132:133], v[222:223], v[132:133], v[98:99]
	s_nop 0
	v_pk_fma_f32 v[130:131], v[224:225], v[130:131], v[132:133]
	v_cvt_f32_i32_e32 v133, v16
	v_cvt_f32_i32_e32 v132, v40
	s_nop 0
	s_nop 0
	v_mov_b32_dpp v134, v128 row_ror:2 row_mask:0xf bank_mask:0xf
	s_nop 0
	v_mov_b32_dpp v135, v129 row_ror:2 row_mask:0xf bank_mask:0xf
	v_pk_mul_f32 v[132:133], v[168:169], v[132:133] op_sel_hi:[0,1]
	v_mov_b32_dpp v106, v128 row_ror:1 row_mask:0xf bank_mask:0xf
	v_mov_b32_dpp v107, v129 row_ror:1 row_mask:0xf bank_mask:0xf
	v_mov_b32_dpp v134, v132 row_shr:2 row_mask:0xf bank_mask:0xf
	v_mov_b32_dpp v135, v133 row_shr:2 row_mask:0xf bank_mask:0xf
	v_mov_b32_dpp v106, v132 row_shr:1 row_mask:0xf bank_mask:0xf
	v_mov_b32_dpp v107, v133 row_shr:1 row_mask:0xf bank_mask:0xf
	v_pk_fma_f32 v[134:135], v[120:121], v[134:135], v[122:123]
	s_nop 0
	v_pk_fma_f32 v[106:107], v[144:145], v[106:107], v[134:135]
	v_cvt_f32_i32_e32 v135, v17
	v_cvt_f32_i32_e32 v134, v41
	s_nop 0
	v_pk_fma_f32 v[104:105], v[232:233], v[118:119], v[104:105]
	s_nop 0
	s_nop 0
	v_mov_b32_dpp v128, v110 row_ror:1 row_mask:0xf bank_mask:0xf
	v_mov_b32_dpp v136, v110 row_ror:2 row_mask:0xf bank_mask:0xf
	v_mov_b32_dpp v129, v111 row_ror:1 row_mask:0xf bank_mask:0xf
	v_mov_b32_dpp v137, v111 row_ror:2 row_mask:0xf bank_mask:0xf
	v_pk_mul_f32 v[110:111], v[168:169], v[134:135] op_sel_hi:[0,1]
	v_mul_f32_e32 v134, 0xbfb8aa3b, v104
	v_exp_f32_e32 v207, v134
	v_mov_b32_dpp v136, v110 row_shr:2 row_mask:0xf bank_mask:0xf
	v_mov_b32_dpp v137, v111 row_shr:2 row_mask:0xf bank_mask:0xf
	v_mov_b32_dpp v128, v110 row_shr:1 row_mask:0xf bank_mask:0xf
	v_mov_b32_dpp v129, v111 row_shr:1 row_mask:0xf bank_mask:0xf
	v_pk_fma_f32 v[134:135], v[142:143], v[136:137], v[100:101]
	v_pk_fma_f32 v[130:131], v[108:109], v[226:227], v[130:131]
	v_pk_fma_f32 v[128:129], v[220:221], v[128:129], v[134:135]
	v_add_f32_e32 v134, 1.0, v207
	v_rcp_f32_e32 v134, v134
	v_mul_f32_e32 v135, 0xbfb8aa3b, v130
	v_exp_f32_e32 v135, v135
	v_pk_fma_f32 v[106:107], v[132:133], v[146:147], v[106:107]
	v_mul_f32_e32 v104, v104, v134
	v_pk_fma_f32 v[128:129], v[110:111], v[140:141], v[128:129]
	v_mul_f32_e32 v104, v104, v105
	v_add_f32_e32 v105, 1.0, v135
	v_mul_f32_e32 v134, 0xbfb8aa3b, v106
	v_rcp_f32_e32 v105, v105
	v_exp_f32_e32 v134, v134
	v_mul_f32_e32 v135, 0xbfb8aa3b, v128
	v_exp_f32_e32 v135, v135
	v_mul_f32_e32 v105, v130, v105
	v_add_f32_e32 v130, 1.0, v134
	v_rcp_f32_e32 v130, v130
	v_add_f32_e32 v134, 1.0, v135
	v_rcp_f32_e32 v134, v134
	v_mul_f32_e32 v105, v105, v131
	v_mul_f32_e32 v106, v106, v130
	v_mul_f32_e32 v106, v106, v107
	v_mul_f32_e32 v107, v128, v134
	v_mul_f32_e32 v107, v107, v129
	v_cvt_pk_bf16_f32 v104, v104, v105
	v_cvt_pk_bf16_f32 v105, v106, v107
	v_add_u32_e32 v106, 32, v169
	v_mad_u64_u32 v[128:129], s[34:35], v106, s72, v[138:139]
	s_nop 0
	s_nop 0
	global_store_dwordx2 v[128:129], v[104:105], off
	s_nop 0
	v_mov_b32_dpp v106, v232 row_ror:2 row_mask:0xf bank_mask:0xf
	s_nop 0
	v_mov_b32_dpp v107, v233 row_ror:2 row_mask:0xf bank_mask:0xf
	v_pk_mul_f32 v[234:235], v[174:175], v[190:191] op_sel_hi:[0,1]
	v_mov_b32_dpp v104, v232 row_ror:1 row_mask:0xf bank_mask:0xf
	v_mov_b32_dpp v105, v233 row_ror:1 row_mask:0xf bank_mask:0xf
	v_mov_b32_dpp v106, v234 row_shr:2 row_mask:0xf bank_mask:0xf
	v_mov_b32_dpp v107, v235 row_shr:2 row_mask:0xf bank_mask:0xf
	s_nop 0
	v_mov_b32_dpp v104, v234 row_shr:1 row_mask:0xf bank_mask:0xf
	v_mov_b32_dpp v105, v235 row_shr:1 row_mask:0xf bank_mask:0xf
	v_pk_fma_f32 v[106:107], v[112:113], v[106:107], v[114:115]
	s_nop 0
	s_nop 0
	v_mov_b32_dpp v134, v108 row_ror:2 row_mask:0xf bank_mask:0xf
	v_pk_fma_f32 v[104:105], v[116:117], v[104:105], v[106:107]
	s_nop 0
	v_mov_b32_dpp v135, v109 row_ror:2 row_mask:0xf bank_mask:0xf
	v_pk_mul_f32 v[106:107], v[174:175], v[186:187] op_sel_hi:[0,1]
	v_mov_b32_dpp v130, v108 row_ror:1 row_mask:0xf bank_mask:0xf
	v_mov_b32_dpp v131, v109 row_ror:1 row_mask:0xf bank_mask:0xf
	v_mov_b32_dpp v134, v106 row_shr:2 row_mask:0xf bank_mask:0xf
	v_mov_b32_dpp v135, v107 row_shr:2 row_mask:0xf bank_mask:0xf
	v_mov_b32_dpp v130, v106 row_shr:1 row_mask:0xf bank_mask:0xf
	v_mov_b32_dpp v131, v107 row_shr:1 row_mask:0xf bank_mask:0xf
	v_pk_fma_f32 v[134:135], v[222:223], v[134:135], v[98:99]
	s_nop 0
	v_pk_fma_f32 v[130:131], v[224:225], v[130:131], v[134:135]
	s_nop 0
	s_nop 0
	v_mov_b32_dpp v136, v132 row_ror:2 row_mask:0xf bank_mask:0xf
	v_pk_fma_f32 v[106:107], v[106:107], v[226:227], v[130:131]
	s_nop 0
	v_mov_b32_dpp v137, v133 row_ror:2 row_mask:0xf bank_mask:0xf
	v_pk_mul_f32 v[130:131], v[174:175], v[188:189] op_sel_hi:[0,1]
	v_mov_b32_dpp v108, v132 row_ror:1 row_mask:0xf bank_mask:0xf
	v_mov_b32_dpp v109, v133 row_ror:1 row_mask:0xf bank_mask:0xf
	v_mov_b32_dpp v136, v130 row_shr:2 row_mask:0xf bank_mask:0xf
	v_mov_b32_dpp v137, v131 row_shr:2 row_mask:0xf bank_mask:0xf
	v_mov_b32_dpp v108, v130 row_shr:1 row_mask:0xf bank_mask:0xf
	v_mov_b32_dpp v109, v131 row_shr:1 row_mask:0xf bank_mask:0xf
	v_pk_fma_f32 v[134:135], v[120:121], v[136:137], v[122:123]
	v_pk_fma_f32 v[104:105], v[234:235], v[118:119], v[104:105]
	v_pk_fma_f32 v[108:109], v[144:145], v[108:109], v[134:135]
	s_nop 0
	v_pk_fma_f32 v[108:109], v[130:131], v[146:147], v[108:109]
	v_mul_f32_e32 v130, 0xbfb8aa3b, v104
	s_nop 0
	s_nop 0
	s_nop 0
	v_exp_f32_e32 v134, v130
	v_mov_b32_dpp v132, v110 row_ror:1 row_mask:0xf bank_mask:0xf
	v_mov_b32_dpp v232, v110 row_ror:2 row_mask:0xf bank_mask:0xf
	v_mov_b32_dpp v133, v111 row_ror:1 row_mask:0xf bank_mask:0xf
	v_mov_b32_dpp v233, v111 row_ror:2 row_mask:0xf bank_mask:0xf
	v_pk_mul_f32 v[110:111], v[174:175], v[184:185] op_sel_hi:[0,1]
	v_add_u32_e32 v103, s61, v103
	v_mov_b32_e32 v102, 0
	v_mov_b32_dpp v232, v110 row_shr:2 row_mask:0xf bank_mask:0xf
	v_mov_b32_dpp v233, v111 row_shr:2 row_mask:0xf bank_mask:0xf
	v_mov_b32_dpp v132, v110 row_shr:1 row_mask:0xf bank_mask:0xf
	v_mov_b32_dpp v133, v111 row_shr:1 row_mask:0xf bank_mask:0xf
	v_pk_fma_f32 v[130:131], v[142:143], v[232:233], v[100:101]
	v_lshl_add_u32 v195, v103, 9, v195
	v_pk_fma_f32 v[130:131], v[220:221], v[132:133], v[130:131]
	v_add_f32_e32 v132, 1.0, v134
	v_rcp_f32_e32 v132, v132
	v_mul_f32_e32 v133, 0xbfb8aa3b, v106
	v_exp_f32_e32 v133, v133
	v_pk_fma_f32 v[110:111], v[110:111], v[140:141], v[130:131]
	v_mul_f32_e32 v104, v104, v132
	v_mul_f32_e32 v104, v104, v105
	v_add_f32_e32 v105, 1.0, v133
	v_mul_f32_e32 v130, 0xbfb8aa3b, v108
	v_rcp_f32_e32 v105, v105
	v_exp_f32_e32 v130, v130
	v_mul_f32_e32 v131, 0xbfb8aa3b, v110
	v_exp_f32_e32 v131, v131
	v_mul_f32_e32 v105, v106, v105
	v_add_f32_e32 v106, 1.0, v130
	v_rcp_f32_e32 v106, v106
	v_add_f32_e32 v130, 1.0, v131
	v_rcp_f32_e32 v130, v130
	v_mul_f32_e32 v105, v105, v107
	v_mul_f32_e32 v106, v108, v106
	v_mul_f32_e32 v106, v106, v109
	v_mul_f32_e32 v107, v110, v130
	v_mul_f32_e32 v107, v107, v111
	v_cvt_pk_bf16_f32 v104, v104, v105
	v_cvt_pk_bf16_f32 v105, v106, v107
	v_add_u32_e32 v106, 48, v169
	v_mad_u64_u32 v[132:133], s[34:35], v106, s72, v[138:139]
	v_mov_b32_e32 v106, 0
	v_mov_b32_e32 v107, 0
	v_mov_b32_e32 v108, 0
	v_mov_b32_e32 v109, 0
	global_store_dwordx2 v[132:133], v[104:105], off
	s_and_saveexec_b64 s[34:35], vcc
	ds_read_b128 v[106:109], v195
	s_or_b64 exec, exec, s[34:35]
	v_mov_b32_e32 v103, 0
	v_mov_b32_e32 v104, 0
	v_mov_b32_e32 v105, 0
	s_and_saveexec_b64 s[34:35], vcc
	ds_read_b128 v[102:105], v195 offset:512
	s_or_b64 exec, exec, s[34:35]
	v_cvt_f32_i32_e32 v237, v90
	v_cvt_f32_i32_e32 v91, v91
	v_cvt_f32_i32_e32 v90, v95
	v_cvt_f32_i32_e32 v236, v94
	v_mov_b32_e32 v110, v157
	v_mov_b32_e32 v130, v157
	v_mov_b32_e32 v134, v157
	s_waitcnt lgkmcnt(0)
	v_mov_b32_dpp v110, v106 row_ror:1 row_mask:0xf bank_mask:0xf
	v_mov_b32_dpp v130, v106 row_ror:2 row_mask:0xf bank_mask:0xf
	v_mov_b32_e32 v106, v157
	v_mov_b32_e32 v135, v157
	v_mov_b32_dpp v134, v107 row_ror:2 row_mask:0xf bank_mask:0xf
	v_mov_b32_dpp v106, v107 row_ror:1 row_mask:0xf bank_mask:0xf
	v_mov_b32_e32 v111, v157
	v_mov_b32_e32 v131, v157
	v_mov_b32_e32 v107, v157
	v_mov_b32_dpp v135, v103 row_ror:2 row_mask:0xf bank_mask:0xf
	v_pk_mul_f32 v[90:91], v[208:209], v[90:91] op_sel_hi:[0,1]
	v_mov_b32_dpp v111, v102 row_ror:1 row_mask:0xf bank_mask:0xf
	v_mov_b32_dpp v131, v102 row_ror:2 row_mask:0xf bank_mask:0xf
	v_pk_mul_f32 v[236:237], v[208:209], v[236:237] op_sel_hi:[0,1]
	v_mov_b32_dpp v107, v103 row_ror:1 row_mask:0xf bank_mask:0xf
	v_mov_b32_dpp v134, v90 row_shr:2 row_mask:0xf bank_mask:0xf
	v_mov_b32_dpp v135, v91 row_shr:2 row_mask:0xf bank_mask:0xf
	v_cvt_f32_i32_e32 v103, v92
	v_cvt_f32_i32_e32 v102, v96
	v_cvt_f32_i32_e32 v93, v93
	v_cvt_f32_i32_e32 v92, v97
	v_mov_b32_e32 v136, v157
	v_mov_b32_e32 v232, v157
	v_mov_b32_dpp v130, v236 row_shr:2 row_mask:0xf bank_mask:0xf
	v_mov_b32_dpp v131, v237 row_shr:2 row_mask:0xf bank_mask:0xf
	v_mov_b32_dpp v106, v90 row_shr:1 row_mask:0xf bank_mask:0xf
	v_mov_b32_dpp v107, v91 row_shr:1 row_mask:0xf bank_mask:0xf
	v_pk_fma_f32 v[94:95], v[222:223], v[134:135], v[98:99]
	v_mov_b32_dpp v136, v108 row_ror:1 row_mask:0xf bank_mask:0xf
	v_mov_b32_dpp v232, v108 row_ror:2 row_mask:0xf bank_mask:0xf
	v_mov_b32_e32 v108, v157
	v_mov_b32_e32 v234, v157
	v_mov_b32_dpp v110, v236 row_shr:1 row_mask:0xf bank_mask:0xf
	v_mov_b32_dpp v111, v237 row_shr:1 row_mask:0xf bank_mask:0xf
	v_pk_fma_f32 v[130:131], v[112:113], v[130:131], v[114:115]
	v_pk_fma_f32 v[94:95], v[224:225], v[106:107], v[94:95]
	v_mov_b32_dpp v108, v109 row_ror:1 row_mask:0xf bank_mask:0xf
	v_mov_b32_dpp v234, v109 row_ror:2 row_mask:0xf bank_mask:0xf
	v_pk_fma_f32 v[110:111], v[116:117], v[110:111], v[130:131]
	v_pk_fma_f32 v[94:95], v[90:91], v[226:227], v[94:95]
	v_mov_b32_e32 v233, v157
	v_mov_b32_e32 v109, v157
	v_mov_b32_e32 v235, v157
	v_pk_fma_f32 v[110:111], v[236:237], v[118:119], v[110:111]
	v_mov_b32_e32 v137, v157
	v_mov_b32_dpp v233, v104 row_ror:2 row_mask:0xf bank_mask:0xf
	v_pk_mul_f32 v[102:103], v[208:209], v[102:103] op_sel_hi:[0,1]
	v_mov_b32_dpp v109, v105 row_ror:1 row_mask:0xf bank_mask:0xf
	v_mov_b32_dpp v235, v105 row_ror:2 row_mask:0xf bank_mask:0xf
	v_pk_mul_f32 v[92:93], v[208:209], v[92:93] op_sel_hi:[0,1]
	v_mul_f32_e32 v105, 0xbfb8aa3b, v94
	v_mov_b32_dpp v137, v104 row_ror:1 row_mask:0xf bank_mask:0xf
	v_mov_b32_dpp v232, v102 row_shr:2 row_mask:0xf bank_mask:0xf
	v_mov_b32_dpp v233, v103 row_shr:2 row_mask:0xf bank_mask:0xf
	v_mov_b32_dpp v234, v92 row_shr:2 row_mask:0xf bank_mask:0xf
	v_mul_f32_e32 v96, 0xbfb8aa3b, v110
	v_mov_b32_dpp v235, v93 row_shr:2 row_mask:0xf bank_mask:0xf
	v_exp_f32_e32 v105, v105
	v_mov_b32_dpp v136, v102 row_shr:1 row_mask:0xf bank_mask:0xf
	v_mov_b32_dpp v137, v103 row_shr:1 row_mask:0xf bank_mask:0xf
	v_pk_fma_f32 v[106:107], v[120:121], v[232:233], v[122:123]
	v_mov_b32_dpp v108, v92 row_shr:1 row_mask:0xf bank_mask:0xf
	v_mov_b32_dpp v109, v93 row_shr:1 row_mask:0xf bank_mask:0xf
	v_exp_f32_e32 v104, v96
	v_pk_fma_f32 v[96:97], v[142:143], v[234:235], v[100:101]
	v_pk_fma_f32 v[106:107], v[144:145], v[136:137], v[106:107]
	v_pk_fma_f32 v[96:97], v[220:221], v[108:109], v[96:97]
	v_pk_fma_f32 v[106:107], v[102:103], v[146:147], v[106:107]
	v_pk_fma_f32 v[96:97], v[92:93], v[140:141], v[96:97]
	v_add_f32_e32 v105, 1.0, v105
	v_mul_f32_e32 v108, 0xbfb8aa3b, v106
	v_mul_f32_e32 v109, 0xbfb8aa3b, v96
	v_rcp_f32_e32 v105, v105
	v_exp_f32_e32 v108, v108
	v_exp_f32_e32 v109, v109
	v_add_f32_e32 v104, 1.0, v104
	v_mul_f32_e32 v94, v94, v105
	v_add_f32_e32 v105, 1.0, v108
	v_add_f32_e32 v108, 1.0, v109
	v_rcp_f32_e32 v105, v105
	v_rcp_f32_e32 v108, v108
	v_rcp_f32_e32 v104, v104
	v_cvt_f32_i32_e32 v135, v82
	v_cvt_f32_i32_e32 v134, v86
	v_mul_f32_e32 v94, v94, v95
	v_mul_f32_e32 v95, v106, v105
	v_mul_f32_e32 v96, v96, v108
	v_add_u32_e32 v207, 0x80, v169
	v_mul_f32_e32 v104, v110, v104
	v_mul_f32_e32 v95, v95, v107
	v_mul_f32_e32 v96, v96, v97
	v_mul_f32_e32 v104, v104, v111
	v_cvt_pk_bf16_f32 v94, v104, v94
	v_cvt_pk_bf16_f32 v95, v95, v96
	v_mad_u64_u32 v[130:131], s[34:35], v207, s72, v[138:139]
	v_mov_b32_e32 v96, v157
	v_mov_b32_e32 v97, v157
	global_store_dwordx2 v[130:131], v[94:95], off
	v_mov_b32_e32 v94, v157
	v_mov_b32_dpp v96, v236 row_ror:2 row_mask:0xf bank_mask:0xf
	v_mov_b32_e32 v95, v157
	v_mov_b32_dpp v97, v237 row_ror:2 row_mask:0xf bank_mask:0xf
	v_pk_mul_f32 v[136:137], v[206:207], v[134:135] op_sel_hi:[0,1]
	v_mov_b32_dpp v94, v236 row_ror:1 row_mask:0xf bank_mask:0xf
	v_mov_b32_dpp v95, v237 row_ror:1 row_mask:0xf bank_mask:0xf
	v_mov_b32_dpp v96, v136 row_shr:2 row_mask:0xf bank_mask:0xf
	v_mov_b32_dpp v97, v137 row_shr:2 row_mask:0xf bank_mask:0xf
	v_mov_b32_dpp v94, v136 row_shr:1 row_mask:0xf bank_mask:0xf
	v_mov_b32_dpp v95, v137 row_shr:1 row_mask:0xf bank_mask:0xf
	v_pk_fma_f32 v[96:97], v[112:113], v[96:97], v[114:115]
	v_cvt_f32_i32_e32 v83, v83
	v_cvt_f32_i32_e32 v82, v87
	v_mov_b32_e32 v104, v157
	v_mov_b32_e32 v106, v157
	v_pk_fma_f32 v[94:95], v[116:117], v[94:95], v[96:97]
	v_mov_b32_dpp v104, v90 row_ror:1 row_mask:0xf bank_mask:0xf
	v_mov_b32_dpp v106, v90 row_ror:2 row_mask:0xf bank_mask:0xf
	v_mov_b32_e32 v90, v157
	v_mov_b32_e32 v108, v157
	v_pk_fma_f32 v[94:95], v[136:137], v[118:119], v[94:95]
	v_mov_b32_dpp v90, v102 row_ror:1 row_mask:0xf bank_mask:0xf
	v_mov_b32_dpp v108, v102 row_ror:2 row_mask:0xf bank_mask:0xf
	v_mov_b32_e32 v102, v157
	v_mov_b32_e32 v110, v157
	v_mov_b32_e32 v107, v157
	v_cvt_f32_i32_e32 v96, v88
	v_mul_f32_e32 v88, 0xbfb8aa3b, v94
	v_mov_b32_dpp v102, v92 row_ror:1 row_mask:0xf bank_mask:0xf
	v_mov_b32_dpp v110, v92 row_ror:2 row_mask:0xf bank_mask:0xf
	v_mov_b32_e32 v105, v157
	v_mov_b32_dpp v107, v91 row_ror:2 row_mask:0xf bank_mask:0xf
	v_pk_mul_f32 v[82:83], v[206:207], v[82:83] op_sel_hi:[0,1]
	v_exp_f32_e32 v92, v88
	v_mov_b32_dpp v105, v91 row_ror:1 row_mask:0xf bank_mask:0xf
	v_mov_b32_dpp v106, v82 row_shr:2 row_mask:0xf bank_mask:0xf
	v_mov_b32_dpp v107, v83 row_shr:2 row_mask:0xf bank_mask:0xf
	v_cvt_f32_i32_e32 v97, v84
	v_cvt_f32_i32_e32 v85, v85
	v_cvt_f32_i32_e32 v84, v89
	v_mov_b32_dpp v104, v82 row_shr:1 row_mask:0xf bank_mask:0xf
	v_mov_b32_dpp v105, v83 row_shr:1 row_mask:0xf bank_mask:0xf
	v_pk_fma_f32 v[86:87], v[222:223], v[106:107], v[98:99]
	v_mov_b32_e32 v91, v157
	v_pk_fma_f32 v[86:87], v[224:225], v[104:105], v[86:87]
	v_mov_b32_e32 v109, v157
	v_pk_fma_f32 v[86:87], v[82:83], v[226:227], v[86:87]
	v_mov_b32_dpp v91, v103 row_ror:1 row_mask:0xf bank_mask:0xf
	v_mov_b32_dpp v109, v103 row_ror:2 row_mask:0xf bank_mask:0xf
	v_mov_b32_e32 v103, v157
	v_mov_b32_e32 v111, v157
	v_add_f32_e32 v92, 1.0, v92
	v_pk_mul_f32 v[96:97], v[206:207], v[96:97] op_sel_hi:[0,1]
	v_mov_b32_dpp v103, v93 row_ror:1 row_mask:0xf bank_mask:0xf
	v_mov_b32_dpp v111, v93 row_ror:2 row_mask:0xf bank_mask:0xf
	v_pk_mul_f32 v[84:85], v[206:207], v[84:85] op_sel_hi:[0,1]
	v_rcp_f32_e32 v92, v92
	v_mul_f32_e32 v93, 0xbfb8aa3b, v86
	v_mov_b32_dpp v108, v96 row_shr:2 row_mask:0xf bank_mask:0xf
	v_mov_b32_dpp v109, v97 row_shr:2 row_mask:0xf bank_mask:0xf
	v_mov_b32_dpp v110, v84 row_shr:2 row_mask:0xf bank_mask:0xf
	v_mov_b32_dpp v111, v85 row_shr:2 row_mask:0xf bank_mask:0xf
	v_exp_f32_e32 v93, v93
	v_mov_b32_dpp v90, v96 row_shr:1 row_mask:0xf bank_mask:0xf
	v_mov_b32_dpp v91, v97 row_shr:1 row_mask:0xf bank_mask:0xf
	v_pk_fma_f32 v[104:105], v[120:121], v[108:109], v[122:123]
	v_mov_b32_dpp v102, v84 row_shr:1 row_mask:0xf bank_mask:0xf
	v_mov_b32_dpp v103, v85 row_shr:1 row_mask:0xf bank_mask:0xf
	v_pk_fma_f32 v[88:89], v[142:143], v[110:111], v[100:101]
	v_pk_fma_f32 v[90:91], v[144:145], v[90:91], v[104:105]
	v_pk_fma_f32 v[88:89], v[220:221], v[102:103], v[88:89]
	v_pk_fma_f32 v[90:91], v[96:97], v[146:147], v[90:91]
	v_pk_fma_f32 v[88:89], v[84:85], v[140:141], v[88:89]
	v_mul_f32_e32 v92, v94, v92
	v_mul_f32_e32 v92, v92, v95
	v_add_f32_e32 v93, 1.0, v93
	v_mul_f32_e32 v94, 0xbfb8aa3b, v90
	v_mul_f32_e32 v95, 0xbfb8aa3b, v88
	v_rcp_f32_e32 v93, v93
	v_exp_f32_e32 v94, v94
	v_exp_f32_e32 v95, v95
	v_cvt_f32_i32_e32 v105, v74
	v_mul_f32_e32 v86, v86, v93
	v_add_f32_e32 v93, 1.0, v94
	v_add_f32_e32 v94, 1.0, v95
	v_rcp_f32_e32 v93, v93
	v_rcp_f32_e32 v94, v94
	v_mul_f32_e32 v86, v86, v87
	v_cvt_f32_i32_e32 v104, v78
	v_mul_f32_e32 v87, v90, v93
	v_mul_f32_e32 v88, v88, v94
	v_mul_f32_e32 v87, v87, v91
	v_mul_f32_e32 v88, v88, v89
	v_cvt_pk_bf16_f32 v86, v92, v86
	v_cvt_pk_bf16_f32 v87, v87, v88
	v_add_u32_e32 v88, 0x90, v169
	v_mad_u64_u32 v[134:135], s[34:35], v88, s72, v[138:139]
	v_mov_b32_e32 v88, v157
	v_mov_b32_e32 v89, v157
	global_store_dwordx2 v[134:135], v[86:87], off
	v_mov_b32_e32 v86, v157
	v_mov_b32_dpp v88, v136 row_ror:2 row_mask:0xf bank_mask:0xf
	v_mov_b32_e32 v87, v157
	v_mov_b32_dpp v89, v137 row_ror:2 row_mask:0xf bank_mask:0xf
	v_pk_mul_f32 v[104:105], v[198:199], v[104:105] op_sel_hi:[0,1]
	v_mov_b32_dpp v86, v136 row_ror:1 row_mask:0xf bank_mask:0xf
	v_mov_b32_dpp v87, v137 row_ror:1 row_mask:0xf bank_mask:0xf
	v_mov_b32_dpp v88, v104 row_shr:2 row_mask:0xf bank_mask:0xf
	v_mov_b32_dpp v89, v105 row_shr:2 row_mask:0xf bank_mask:0xf
	v_mov_b32_dpp v86, v104 row_shr:1 row_mask:0xf bank_mask:0xf
	v_mov_b32_dpp v87, v105 row_shr:1 row_mask:0xf bank_mask:0xf
	v_pk_fma_f32 v[88:89], v[112:113], v[88:89], v[114:115]
	v_cvt_f32_i32_e32 v75, v75
	v_cvt_f32_i32_e32 v74, v79
	v_mov_b32_e32 v90, v157
	v_mov_b32_e32 v92, v157
	v_pk_fma_f32 v[86:87], v[116:117], v[86:87], v[88:89]
	v_mov_b32_dpp v90, v82 row_ror:1 row_mask:0xf bank_mask:0xf
	v_mov_b32_dpp v92, v82 row_ror:2 row_mask:0xf bank_mask:0xf
	v_mov_b32_e32 v82, v157
	v_mov_b32_e32 v94, v157
	v_pk_fma_f32 v[86:87], v[104:105], v[118:119], v[86:87]
	v_mov_b32_dpp v82, v96 row_ror:1 row_mask:0xf bank_mask:0xf
	v_mov_b32_dpp v94, v96 row_ror:2 row_mask:0xf bank_mask:0xf
	v_mov_b32_e32 v96, v157
	v_mov_b32_e32 v102, v157
	v_mov_b32_e32 v93, v157
	v_cvt_f32_i32_e32 v88, v80
	v_mul_f32_e32 v80, 0xbfb8aa3b, v86
	v_mov_b32_dpp v96, v84 row_ror:1 row_mask:0xf bank_mask:0xf
	v_mov_b32_dpp v102, v84 row_ror:2 row_mask:0xf bank_mask:0xf
	v_mov_b32_e32 v91, v157
	v_mov_b32_dpp v93, v83 row_ror:2 row_mask:0xf bank_mask:0xf
	v_pk_mul_f32 v[74:75], v[198:199], v[74:75] op_sel_hi:[0,1]
	v_exp_f32_e32 v84, v80
	v_mov_b32_dpp v91, v83 row_ror:1 row_mask:0xf bank_mask:0xf
	v_mov_b32_dpp v92, v74 row_shr:2 row_mask:0xf bank_mask:0xf
	v_mov_b32_dpp v93, v75 row_shr:2 row_mask:0xf bank_mask:0xf
	v_cvt_f32_i32_e32 v89, v76
	v_cvt_f32_i32_e32 v77, v77
	v_cvt_f32_i32_e32 v76, v81
	v_mov_b32_dpp v90, v74 row_shr:1 row_mask:0xf bank_mask:0xf
	v_mov_b32_dpp v91, v75 row_shr:1 row_mask:0xf bank_mask:0xf
	v_pk_fma_f32 v[78:79], v[222:223], v[92:93], v[98:99]
	v_mov_b32_e32 v83, v157
	v_pk_fma_f32 v[78:79], v[224:225], v[90:91], v[78:79]
	v_mov_b32_e32 v95, v157
	v_pk_fma_f32 v[78:79], v[74:75], v[226:227], v[78:79]
	v_mov_b32_dpp v83, v97 row_ror:1 row_mask:0xf bank_mask:0xf
	v_mov_b32_dpp v95, v97 row_ror:2 row_mask:0xf bank_mask:0xf
	v_mov_b32_e32 v97, v157
	v_mov_b32_e32 v103, v157
	v_add_f32_e32 v84, 1.0, v84
	v_pk_mul_f32 v[88:89], v[198:199], v[88:89] op_sel_hi:[0,1]
	v_mov_b32_dpp v97, v85 row_ror:1 row_mask:0xf bank_mask:0xf
	v_mov_b32_dpp v103, v85 row_ror:2 row_mask:0xf bank_mask:0xf
	v_pk_mul_f32 v[76:77], v[198:199], v[76:77] op_sel_hi:[0,1]
	v_rcp_f32_e32 v84, v84
	v_mul_f32_e32 v85, 0xbfb8aa3b, v78
	v_mov_b32_dpp v94, v88 row_shr:2 row_mask:0xf bank_mask:0xf
	v_mov_b32_dpp v95, v89 row_shr:2 row_mask:0xf bank_mask:0xf
	v_mov_b32_dpp v102, v76 row_shr:2 row_mask:0xf bank_mask:0xf
	v_mov_b32_dpp v103, v77 row_shr:2 row_mask:0xf bank_mask:0xf
	v_exp_f32_e32 v85, v85
	v_mov_b32_dpp v82, v88 row_shr:1 row_mask:0xf bank_mask:0xf
	v_mov_b32_dpp v83, v89 row_shr:1 row_mask:0xf bank_mask:0xf
	v_pk_fma_f32 v[90:91], v[120:121], v[94:95], v[122:123]
	v_mov_b32_dpp v96, v76 row_shr:1 row_mask:0xf bank_mask:0xf
	v_mov_b32_dpp v97, v77 row_shr:1 row_mask:0xf bank_mask:0xf
	v_pk_fma_f32 v[80:81], v[142:143], v[102:103], v[100:101]
	v_pk_fma_f32 v[82:83], v[144:145], v[82:83], v[90:91]
	v_pk_fma_f32 v[80:81], v[220:221], v[96:97], v[80:81]
	v_pk_fma_f32 v[82:83], v[88:89], v[146:147], v[82:83]
	v_pk_fma_f32 v[80:81], v[76:77], v[140:141], v[80:81]
	v_mul_f32_e32 v84, v86, v84
	v_mul_f32_e32 v84, v84, v87
	v_add_f32_e32 v85, 1.0, v85
	v_mul_f32_e32 v86, 0xbfb8aa3b, v82
	v_mul_f32_e32 v87, 0xbfb8aa3b, v80
	v_rcp_f32_e32 v85, v85
	v_exp_f32_e32 v86, v86
	v_exp_f32_e32 v87, v87
	v_pk_mul_f32 v[92:93], v[194:195], v[218:219] op_sel_hi:[0,1]
	v_mul_f32_e32 v78, v78, v85
	v_add_f32_e32 v85, 1.0, v86
	v_add_f32_e32 v86, 1.0, v87
	v_rcp_f32_e32 v85, v85
	v_rcp_f32_e32 v86, v86
	v_mul_f32_e32 v78, v78, v79
	v_cvt_pk_bf16_f32 v78, v84, v78
	v_mul_f32_e32 v79, v82, v85
	v_mul_f32_e32 v80, v80, v86
	v_mul_f32_e32 v79, v79, v83
	v_mul_f32_e32 v80, v80, v81
	v_cvt_pk_bf16_f32 v79, v79, v80
	v_add_u32_e32 v80, 0xa0, v169
	v_mad_u64_u32 v[136:137], s[34:35], v80, s72, v[138:139]
	v_mov_b32_e32 v80, v157
	v_mov_b32_e32 v81, v157
	global_store_dwordx2 v[136:137], v[78:79], off
	v_mov_b32_e32 v78, v157
	v_mov_b32_dpp v80, v104 row_ror:2 row_mask:0xf bank_mask:0xf
	v_mov_b32_e32 v79, v157
	v_mov_b32_dpp v81, v105 row_ror:2 row_mask:0xf bank_mask:0xf
	v_mov_b32_dpp v78, v104 row_ror:1 row_mask:0xf bank_mask:0xf
	v_mov_b32_dpp v79, v105 row_ror:1 row_mask:0xf bank_mask:0xf
	v_mov_b32_dpp v80, v92 row_shr:2 row_mask:0xf bank_mask:0xf
	v_mov_b32_dpp v81, v93 row_shr:2 row_mask:0xf bank_mask:0xf
	v_mov_b32_e32 v84, v157
	v_mov_b32_dpp v78, v92 row_shr:1 row_mask:0xf bank_mask:0xf
	v_mov_b32_dpp v79, v93 row_shr:1 row_mask:0xf bank_mask:0xf
	v_pk_fma_f32 v[80:81], v[112:113], v[80:81], v[114:115]
	v_mov_b32_e32 v85, v157
	v_mov_b32_e32 v82, v157
	v_mov_b32_dpp v84, v74 row_ror:2 row_mask:0xf bank_mask:0xf
	v_pk_fma_f32 v[78:79], v[116:117], v[78:79], v[80:81]
	v_mov_b32_e32 v83, v157
	v_mov_b32_dpp v85, v75 row_ror:2 row_mask:0xf bank_mask:0xf
	v_pk_mul_f32 v[80:81], v[194:195], v[216:217] op_sel_hi:[0,1]
	v_mov_b32_dpp v82, v74 row_ror:1 row_mask:0xf bank_mask:0xf
	v_mov_b32_dpp v83, v75 row_ror:1 row_mask:0xf bank_mask:0xf
	v_mov_b32_dpp v84, v80 row_shr:2 row_mask:0xf bank_mask:0xf
	v_mov_b32_dpp v85, v81 row_shr:2 row_mask:0xf bank_mask:0xf
	v_mov_b32_dpp v82, v80 row_shr:1 row_mask:0xf bank_mask:0xf
	v_mov_b32_dpp v83, v81 row_shr:1 row_mask:0xf bank_mask:0xf
	v_pk_fma_f32 v[84:85], v[222:223], v[84:85], v[98:99]
	v_mov_b32_e32 v86, v157
	v_pk_fma_f32 v[82:83], v[224:225], v[82:83], v[84:85]
	v_mov_b32_e32 v87, v157
	v_mov_b32_e32 v74, v157
	v_mov_b32_dpp v86, v88 row_ror:2 row_mask:0xf bank_mask:0xf
	v_pk_fma_f32 v[80:81], v[80:81], v[226:227], v[82:83]
	v_mov_b32_e32 v75, v157
	v_mov_b32_dpp v87, v89 row_ror:2 row_mask:0xf bank_mask:0xf
	v_pk_mul_f32 v[82:83], v[194:195], v[214:215] op_sel_hi:[0,1]
	v_mov_b32_dpp v74, v88 row_ror:1 row_mask:0xf bank_mask:0xf
	v_mov_b32_dpp v75, v89 row_ror:1 row_mask:0xf bank_mask:0xf
	v_mov_b32_dpp v86, v82 row_shr:2 row_mask:0xf bank_mask:0xf
	v_mov_b32_dpp v87, v83 row_shr:2 row_mask:0xf bank_mask:0xf
	v_mov_b32_dpp v74, v82 row_shr:1 row_mask:0xf bank_mask:0xf
	v_mov_b32_dpp v75, v83 row_shr:1 row_mask:0xf bank_mask:0xf
	v_pk_fma_f32 v[84:85], v[120:121], v[86:87], v[122:123]
	v_pk_fma_f32 v[78:79], v[92:93], v[118:119], v[78:79]
	v_pk_fma_f32 v[74:75], v[144:145], v[74:75], v[84:85]
	v_mov_b32_e32 v88, v157
	v_pk_fma_f32 v[74:75], v[82:83], v[146:147], v[74:75]
	v_mul_f32_e32 v82, 0xbfb8aa3b, v78
	v_exp_f32_e32 v84, v82
	v_mov_b32_e32 v90, v157
	v_mov_b32_e32 v89, v157
	v_mov_b32_e32 v91, v157
	v_add_f32_e32 v84, 1.0, v84
	v_rcp_f32_e32 v84, v84
	v_mul_f32_e32 v85, 0xbfb8aa3b, v80
	v_mov_b32_dpp v88, v76 row_ror:1 row_mask:0xf bank_mask:0xf
	v_mov_b32_dpp v90, v76 row_ror:2 row_mask:0xf bank_mask:0xf
	v_mov_b32_dpp v89, v77 row_ror:1 row_mask:0xf bank_mask:0xf
	v_mov_b32_dpp v91, v77 row_ror:2 row_mask:0xf bank_mask:0xf
	v_pk_mul_f32 v[76:77], v[194:195], v[210:211] op_sel_hi:[0,1]
	v_exp_f32_e32 v85, v85
	v_mul_f32_e32 v78, v78, v84
	v_mov_b32_dpp v90, v76 row_shr:2 row_mask:0xf bank_mask:0xf
	v_mov_b32_dpp v91, v77 row_shr:2 row_mask:0xf bank_mask:0xf
	v_mov_b32_dpp v88, v76 row_shr:1 row_mask:0xf bank_mask:0xf
	v_mov_b32_dpp v89, v77 row_shr:1 row_mask:0xf bank_mask:0xf
	v_pk_fma_f32 v[82:83], v[142:143], v[90:91], v[100:101]
	v_mul_f32_e32 v78, v78, v79
	v_pk_fma_f32 v[82:83], v[220:221], v[88:89], v[82:83]
	v_add_f32_e32 v79, 1.0, v85
	v_pk_fma_f32 v[76:77], v[76:77], v[140:141], v[82:83]
	v_mul_f32_e32 v82, 0xbfb8aa3b, v74
	v_rcp_f32_e32 v79, v79
	v_exp_f32_e32 v82, v82
	v_mul_f32_e32 v83, 0xbfb8aa3b, v76
	v_exp_f32_e32 v83, v83
	v_mul_f32_e32 v79, v80, v79
	v_add_f32_e32 v80, 1.0, v82
	v_rcp_f32_e32 v80, v80
	v_add_f32_e32 v82, 1.0, v83
	v_rcp_f32_e32 v82, v82
	v_mul_f32_e32 v79, v79, v81
	v_mul_f32_e32 v74, v74, v80
	v_mul_f32_e32 v74, v74, v75
	v_mul_f32_e32 v75, v76, v82
	v_mul_f32_e32 v75, v75, v77
	v_cvt_pk_bf16_f32 v76, v78, v79
	v_cvt_pk_bf16_f32 v77, v74, v75
	v_or_b32_e32 v74, 1, v199
	v_lshl_add_u32 v74, v74, 4, 0
	v_add_u32_e32 v75, 0x22400, v74
	v_add_u32_e32 v78, 0x22000, v74
	ds_read_b128 v[88:91], v75
	ds_read_b128 v[80:83], v78
	ds_read_b128 v[100:103], v78 offset:2048
	ds_read_b128 v[96:99], v78 offset:3072
	ds_read_b128 v[92:95], v78 offset:4096
	v_add_u32_e32 v75, 0xb0, v169
	v_mad_u64_u32 v[138:139], s[34:35], v75, s72, v[138:139]
	global_store_dwordx2 v[138:139], v[76:77], off
	s_and_saveexec_b64 s[34:35], s[0:1]
	s_cbranch_execz .LBB0_1679
	v_cvt_f32_i32_e32 v77, v37
	v_cvt_f32_i32_e32 v85, v35
	v_cvt_f32_i32_e32 v84, v34
	v_cvt_f32_i32_e32 v76, v36
	v_pk_mul_f32 v[84:85], v[172:173], v[84:85] op_sel_hi:[0,1]
	v_pk_mul_f32 v[76:77], v[172:173], v[76:77] op_sel_hi:[0,1]
	s_waitcnt lgkmcnt(4)
	v_pk_mul_f32 v[86:87], v[76:77], v[90:91]
	v_pk_mul_f32 v[84:85], v[84:85], v[88:89]
	v_mad_i64_i32 v[76:77], s[38:39], v173, s73, v[212:213]
	global_store_dwordx4 v[76:77], v[84:87], off offset:16

.LBB0_1681:
	s_or_b64 exec, exec, s[34:35]
	s_nop 0
	v_mov_b32_e32 v84, 0
	v_mov_b32_e32 v112, 0
	v_mov_b32_e32 v113, 0
	v_mov_b32_e32 v114, 0
	v_mov_b32_e32 v115, 0
	s_and_saveexec_b64 s[0:1], s[40:41]
	ds_read_b128 v[112:115], v171 offset:16
	s_or_b64 exec, exec, s[0:1]
	v_mov_b32_e32 v85, 0
	v_mov_b32_e32 v86, 0
	v_mov_b32_e32 v87, 0
	s_and_saveexec_b64 s[0:1], s[40:41]
	ds_read_b128 v[84:87], v171 offset:528
	s_or_b64 exec, exec, s[0:1]
	s_waitcnt lgkmcnt(3)
	v_pk_mul_f32 v[122:123], v[106:107], v[122:123]
	s_waitcnt lgkmcnt(2)
	v_pk_mul_f32 v[118:119], v[106:107], v[118:119]
	s_waitcnt lgkmcnt(0)
	v_pk_mul_f32 v[106:107], v[106:107], v[110:111]
	v_pk_mul_f32 v[100:101], v[88:89], v[100:101]
	v_pk_mul_f32 v[110:111], v[90:91], v[98:99]
	v_pk_mul_f32 v[96:97], v[88:89], v[96:97]
	v_pk_mul_f32 v[98:99], v[88:89], v[92:93]
	v_cvt_f32_i32_e32 v89, v10
	v_cvt_f32_i32_e32 v88, v34
	v_mov_b32_e32 v173, v172
	s_nop 0
	s_nop 0
	v_pk_mul_f32 v[120:121], v[104:105], v[120:121]
	v_mov_b32_dpp v92, v112 row_ror:2 row_mask:0xf bank_mask:0xf
	v_mov_b32_dpp v93, v84 row_ror:2 row_mask:0xf bank_mask:0xf
	v_pk_mul_f32 v[210:211], v[172:173], v[88:89]
	v_cvt_f32_i32_e32 v215, v11
	v_cvt_f32_i32_e32 v214, v35
	v_pk_mul_f32 v[116:117], v[104:105], v[116:117]
	v_pk_mul_f32 v[104:105], v[104:105], v[108:109]
	v_pk_mul_f32 v[108:109], v[90:91], v[102:103]
	v_pk_mul_f32 v[140:141], v[90:91], v[94:95]
	s_nop 0
	v_mov_b32_dpp v92, v210 row_shr:2 row_mask:0xf bank_mask:0xf
	v_mov_b32_dpp v93, v211 row_shr:2 row_mask:0xf bank_mask:0xf
	v_mov_b32_e32 v88, v100
	v_mov_b32_e32 v89, v120
	v_mov_b32_e32 v90, v80
	v_mov_b32_e32 v91, v74
	v_mov_b32_dpp v94, v112 row_ror:1 row_mask:0xf bank_mask:0xf
	s_nop 0
	s_nop 0
	v_pk_fma_f32 v[212:213], v[88:89], v[92:93], v[90:91]
	v_mov_b32_e32 v92, v96
	v_mov_b32_e32 v93, v116
	v_mov_b32_e32 v116, v97
	v_cvt_f32_i32_e32 v97, v12
	v_cvt_f32_i32_e32 v96, v36
	v_mov_b32_dpp v102, v113 row_ror:1 row_mask:0xf bank_mask:0xf
	v_mov_b32_dpp v112, v113 row_ror:2 row_mask:0xf bank_mask:0xf
	s_nop 0
	s_nop 0
	s_nop 0
	v_mov_b32_dpp v95, v84 row_ror:1 row_mask:0xf bank_mask:0xf
	v_mov_b32_dpp v103, v85 row_ror:1 row_mask:0xf bank_mask:0xf
	v_mov_b32_dpp v113, v85 row_ror:2 row_mask:0xf bank_mask:0xf
	v_pk_mul_f32 v[84:85], v[172:173], v[214:215]
	s_nop 0
	v_mov_b32_e32 v120, v101
	v_mov_b32_dpp v112, v84 row_shr:2 row_mask:0xf bank_mask:0xf
	v_mov_b32_dpp v113, v85 row_shr:2 row_mask:0xf bank_mask:0xf
	v_mov_b32_e32 v74, v81
	s_nop 0
	v_mov_b32_dpp v144, v114 row_ror:2 row_mask:0xf bank_mask:0xf
	v_mov_b32_dpp v94, v210 row_shr:1 row_mask:0xf bank_mask:0xf
	v_mov_b32_dpp v95, v211 row_shr:1 row_mask:0xf bank_mask:0xf
	v_pk_fma_f32 v[80:81], v[120:121], v[112:113], v[74:75]
	v_mov_b32_dpp v145, v86 row_ror:2 row_mask:0xf bank_mask:0xf
	v_pk_mul_f32 v[112:113], v[172:173], v[96:97]
	v_pk_fma_f32 v[212:213], v[92:93], v[94:95], v[212:213]
	v_mov_b32_e32 v94, v98
	v_mov_b32_e32 v95, v104
	v_mov_b32_dpp v102, v84 row_shr:1 row_mask:0xf bank_mask:0xf
	v_mov_b32_dpp v103, v85 row_shr:1 row_mask:0xf bank_mask:0xf
	v_mov_b32_e32 v104, v99
	v_mov_b32_dpp v144, v112 row_shr:2 row_mask:0xf bank_mask:0xf
	v_mov_b32_dpp v145, v113 row_shr:2 row_mask:0xf bank_mask:0xf
	v_mov_b32_e32 v96, v108
	v_mov_b32_e32 v97, v122
	v_mov_b32_e32 v98, v82
	v_mov_b32_e32 v99, v76
	v_pk_fma_f32 v[80:81], v[116:117], v[102:103], v[80:81]
	v_pk_fma_f32 v[102:103], v[96:97], v[144:145], v[98:99]
	v_cvt_f32_i32_e32 v145, v13
	v_cvt_f32_i32_e32 v144, v37
	s_nop 0
	s_nop 0
	v_pk_fma_f32 v[80:81], v[84:85], v[104:105], v[80:81]
	v_mov_b32_dpp v142, v114 row_ror:1 row_mask:0xf bank_mask:0xf
	s_nop 0
	v_mov_b32_dpp v146, v115 row_ror:2 row_mask:0xf bank_mask:0xf
	s_nop 0
	v_mov_b32_dpp v114, v115 row_ror:1 row_mask:0xf bank_mask:0xf
	s_nop 0
	s_nop 0
	v_mov_b32_dpp v143, v86 row_ror:1 row_mask:0xf bank_mask:0xf
	v_mov_b32_dpp v115, v87 row_ror:1 row_mask:0xf bank_mask:0xf
	v_mov_b32_dpp v147, v87 row_ror:2 row_mask:0xf bank_mask:0xf
	v_pk_mul_f32 v[86:87], v[172:173], v[144:145]
	v_mul_f32_e32 v108, 0xbfb8aa3b, v80
	v_mov_b32_e32 v122, v109
	v_mov_b32_dpp v146, v86 row_shr:2 row_mask:0xf bank_mask:0xf
	v_mov_b32_dpp v147, v87 row_shr:2 row_mask:0xf bank_mask:0xf
	v_mov_b32_e32 v76, v83
	v_exp_f32_e32 v108, v108
	v_mov_b32_dpp v142, v112 row_shr:1 row_mask:0xf bank_mask:0xf
	v_mov_b32_dpp v143, v113 row_shr:1 row_mask:0xf bank_mask:0xf
	v_mov_b32_e32 v100, v110
	v_mov_b32_e32 v101, v118
	v_mov_b32_dpp v114, v86 row_shr:1 row_mask:0xf bank_mask:0xf
	v_mov_b32_dpp v115, v87 row_shr:1 row_mask:0xf bank_mask:0xf
	v_pk_fma_f32 v[82:83], v[122:123], v[146:147], v[76:77]
	v_mov_b32_e32 v118, v111
	v_pk_fma_f32 v[142:143], v[100:101], v[142:143], v[102:103]
	v_mov_b32_e32 v102, v140
	v_mov_b32_e32 v103, v106
	v_pk_fma_f32 v[82:83], v[118:119], v[114:115], v[82:83]
	v_mov_b32_e32 v106, v141
	v_pk_fma_f32 v[142:143], v[112:113], v[102:103], v[142:143]
	v_pk_fma_f32 v[82:83], v[86:87], v[106:107], v[82:83]
	v_pk_fma_f32 v[212:213], v[210:211], v[94:95], v[212:213]
	v_add_f32_e32 v108, 1.0, v108
	v_mul_f32_e32 v109, 0xbfb8aa3b, v142
	v_mul_f32_e32 v110, 0xbfb8aa3b, v82
	v_mul_f32_e32 v79, 0xbfb8aa3b, v212
	v_rcp_f32_e32 v108, v108
	v_exp_f32_e32 v109, v109
	v_exp_f32_e32 v110, v110
	v_exp_f32_e32 v79, v79
	v_mul_f32_e32 v80, v80, v108
	v_add_f32_e32 v108, 1.0, v109
	v_add_f32_e32 v109, 1.0, v110
	v_add_f32_e32 v79, 1.0, v79
	v_rcp_f32_e32 v108, v108
	v_rcp_f32_e32 v109, v109
	v_rcp_f32_e32 v79, v79
	v_cvt_f32_i32_e32 v141, v6
	v_cvt_f32_i32_e32 v140, v30
	v_mul_f32_e32 v80, v80, v81
	v_mul_f32_e32 v81, v142, v108
	v_mul_f32_e32 v82, v82, v109
	v_mul_f32_e32 v79, v212, v79
	v_mul_f32_e32 v81, v81, v143
	v_mul_f32_e32 v82, v82, v83
	v_mov_b32_e32 v171, v170
	v_mul_f32_e32 v79, v79, v213
	v_cvt_pk_bf16_f32 v80, v79, v80
	v_cvt_pk_bf16_f32 v81, v81, v82
	s_nop 0
	s_nop 0
	global_store_dwordx2 v[124:125], v[80:81], off offset:8
	s_nop 0
	v_mov_b32_dpp v82, v210 row_ror:2 row_mask:0xf bank_mask:0xf
	s_nop 0
	v_mov_b32_dpp v83, v211 row_ror:2 row_mask:0xf bank_mask:0xf
	v_pk_mul_f32 v[140:141], v[170:171], v[140:141]
	v_mov_b32_dpp v80, v210 row_ror:1 row_mask:0xf bank_mask:0xf
	v_mov_b32_dpp v81, v211 row_ror:1 row_mask:0xf bank_mask:0xf
	v_mov_b32_dpp v82, v140 row_shr:2 row_mask:0xf bank_mask:0xf
	v_mov_b32_dpp v83, v141 row_shr:2 row_mask:0xf bank_mask:0xf
	v_mov_b32_dpp v80, v140 row_shr:1 row_mask:0xf bank_mask:0xf
	v_mov_b32_dpp v81, v141 row_shr:1 row_mask:0xf bank_mask:0xf
	v_pk_fma_f32 v[82:83], v[88:89], v[82:83], v[90:91]
	s_nop 0
	v_pk_fma_f32 v[80:81], v[92:93], v[80:81], v[82:83]
	v_cvt_f32_i32_e32 v83, v7
	v_cvt_f32_i32_e32 v82, v31
	s_nop 0
	s_nop 0
	v_mov_b32_dpp v110, v84 row_ror:2 row_mask:0xf bank_mask:0xf
	s_nop 0
	v_mov_b32_dpp v111, v85 row_ror:2 row_mask:0xf bank_mask:0xf
	v_pk_mul_f32 v[82:83], v[170:171], v[82:83]
	v_mov_b32_dpp v108, v84 row_ror:1 row_mask:0xf bank_mask:0xf
	v_mov_b32_dpp v109, v85 row_ror:1 row_mask:0xf bank_mask:0xf
	v_mov_b32_dpp v110, v82 row_shr:2 row_mask:0xf bank_mask:0xf
	v_mov_b32_dpp v111, v83 row_shr:2 row_mask:0xf bank_mask:0xf
	v_mov_b32_dpp v108, v82 row_shr:1 row_mask:0xf bank_mask:0xf
	v_mov_b32_dpp v109, v83 row_shr:1 row_mask:0xf bank_mask:0xf
	v_pk_fma_f32 v[110:111], v[120:121], v[110:111], v[74:75]
	s_nop 0
	v_pk_fma_f32 v[108:109], v[116:117], v[108:109], v[110:111]
	v_cvt_f32_i32_e32 v111, v8
	v_cvt_f32_i32_e32 v110, v32
	s_nop 0
	s_nop 0
	v_mov_b32_dpp v114, v112 row_ror:2 row_mask:0xf bank_mask:0xf
	s_nop 0
	v_mov_b32_dpp v115, v113 row_ror:2 row_mask:0xf bank_mask:0xf
	v_pk_mul_f32 v[110:111], v[170:171], v[110:111]
	v_mov_b32_dpp v84, v112 row_ror:1 row_mask:0xf bank_mask:0xf
	v_mov_b32_dpp v85, v113 row_ror:1 row_mask:0xf bank_mask:0xf
	v_mov_b32_dpp v114, v110 row_shr:2 row_mask:0xf bank_mask:0xf
	v_mov_b32_dpp v115, v111 row_shr:2 row_mask:0xf bank_mask:0xf
	v_pk_fma_f32 v[80:81], v[140:141], v[94:95], v[80:81]
	v_mov_b32_dpp v84, v110 row_shr:1 row_mask:0xf bank_mask:0xf
	v_mov_b32_dpp v85, v111 row_shr:1 row_mask:0xf bank_mask:0xf
	v_pk_fma_f32 v[114:115], v[96:97], v[114:115], v[98:99]
	v_mul_f32_e32 v79, 0xbfb8aa3b, v80
	v_pk_fma_f32 v[84:85], v[100:101], v[84:85], v[114:115]
	v_cvt_f32_i32_e32 v115, v9
	v_cvt_f32_i32_e32 v114, v33
	v_exp_f32_e32 v79, v79
	s_nop 0
	s_nop 0
	s_nop 0
	s_nop 0
	v_mov_b32_dpp v112, v86 row_ror:1 row_mask:0xf bank_mask:0xf
	v_mov_b32_dpp v124, v86 row_ror:2 row_mask:0xf bank_mask:0xf
	v_mov_b32_dpp v113, v87 row_ror:1 row_mask:0xf bank_mask:0xf
	v_mov_b32_dpp v125, v87 row_ror:2 row_mask:0xf bank_mask:0xf
	v_pk_mul_f32 v[86:87], v[170:171], v[114:115]
	v_add_f32_e32 v79, 1.0, v79
	v_pk_fma_f32 v[108:109], v[82:83], v[104:105], v[108:109]
	v_mov_b32_dpp v124, v86 row_shr:2 row_mask:0xf bank_mask:0xf
	v_mov_b32_dpp v125, v87 row_shr:2 row_mask:0xf bank_mask:0xf
	v_mov_b32_dpp v112, v86 row_shr:1 row_mask:0xf bank_mask:0xf
	v_mov_b32_dpp v113, v87 row_shr:1 row_mask:0xf bank_mask:0xf
	v_pk_fma_f32 v[114:115], v[122:123], v[124:125], v[76:77]
	v_rcp_f32_e32 v79, v79
	v_pk_fma_f32 v[112:113], v[118:119], v[112:113], v[114:115]
	v_mul_f32_e32 v114, 0xbfb8aa3b, v108
	v_exp_f32_e32 v114, v114
	v_pk_fma_f32 v[84:85], v[110:111], v[102:103], v[84:85]
	v_mul_f32_e32 v79, v80, v79
	v_pk_fma_f32 v[112:113], v[86:87], v[106:107], v[112:113]
	v_mul_f32_e32 v79, v79, v81
	v_mul_f32_e32 v81, 0xbfb8aa3b, v84
	v_add_f32_e32 v80, 1.0, v114
	v_exp_f32_e32 v81, v81
	v_mul_f32_e32 v114, 0xbfb8aa3b, v112
	v_rcp_f32_e32 v80, v80
	v_exp_f32_e32 v114, v114
	v_add_f32_e32 v81, 1.0, v81
	v_rcp_f32_e32 v81, v81
	v_mul_f32_e32 v80, v108, v80
	v_add_f32_e32 v108, 1.0, v114
	v_rcp_f32_e32 v108, v108
	v_mul_f32_e32 v81, v84, v81
	v_mul_f32_e32 v80, v80, v109
	v_mul_f32_e32 v81, v81, v85
	v_mul_f32_e32 v84, v112, v108
	v_mul_f32_e32 v84, v84, v113
	v_cvt_pk_bf16_f32 v80, v79, v80
	v_cvt_pk_bf16_f32 v81, v81, v84
	global_store_dwordx2 v[126:127], v[80:81], off offset:8
	v_cvt_f32_i32_e32 v127, v2
	v_cvt_f32_i32_e32 v126, v26
	v_mov_b32_e32 v169, v168
	s_nop 0
	s_nop 0
	s_nop 0
	v_mov_b32_dpp v84, v140 row_ror:2 row_mask:0xf bank_mask:0xf
	s_nop 0
	v_mov_b32_dpp v85, v141 row_ror:2 row_mask:0xf bank_mask:0xf
	v_pk_mul_f32 v[126:127], v[168:169], v[126:127]
	v_mov_b32_dpp v80, v140 row_ror:1 row_mask:0xf bank_mask:0xf
	v_mov_b32_dpp v81, v141 row_ror:1 row_mask:0xf bank_mask:0xf
	v_mov_b32_dpp v84, v126 row_shr:2 row_mask:0xf bank_mask:0xf
	v_mov_b32_dpp v85, v127 row_shr:2 row_mask:0xf bank_mask:0xf
	v_mov_b32_dpp v80, v126 row_shr:1 row_mask:0xf bank_mask:0xf
	v_mov_b32_dpp v81, v127 row_shr:1 row_mask:0xf bank_mask:0xf
	v_pk_fma_f32 v[84:85], v[88:89], v[84:85], v[90:91]
	s_nop 0
	v_pk_fma_f32 v[80:81], v[92:93], v[80:81], v[84:85]
	v_cvt_f32_i32_e32 v85, v3
	v_cvt_f32_i32_e32 v84, v27
	s_nop 0
	s_nop 0
	v_mov_b32_dpp v112, v82 row_ror:2 row_mask:0xf bank_mask:0xf
	s_nop 0
	v_mov_b32_dpp v113, v83 row_ror:2 row_mask:0xf bank_mask:0xf
	v_pk_mul_f32 v[84:85], v[168:169], v[84:85]
	v_mov_b32_dpp v108, v82 row_ror:1 row_mask:0xf bank_mask:0xf
	v_mov_b32_dpp v109, v83 row_ror:1 row_mask:0xf bank_mask:0xf
	v_mov_b32_dpp v112, v84 row_shr:2 row_mask:0xf bank_mask:0xf
	v_mov_b32_dpp v113, v85 row_shr:2 row_mask:0xf bank_mask:0xf
	v_mov_b32_dpp v108, v84 row_shr:1 row_mask:0xf bank_mask:0xf
	v_mov_b32_dpp v109, v85 row_shr:1 row_mask:0xf bank_mask:0xf
	v_pk_fma_f32 v[112:113], v[120:121], v[112:113], v[74:75]
	s_nop 0
	v_pk_fma_f32 v[108:109], v[116:117], v[108:109], v[112:113]
	v_cvt_f32_i32_e32 v113, v4
	v_cvt_f32_i32_e32 v112, v28
	s_nop 0
	s_nop 0
	v_mov_b32_dpp v114, v110 row_ror:2 row_mask:0xf bank_mask:0xf
	s_nop 0
	v_mov_b32_dpp v115, v111 row_ror:2 row_mask:0xf bank_mask:0xf
	v_pk_mul_f32 v[112:113], v[168:169], v[112:113]
	v_mov_b32_dpp v82, v110 row_ror:1 row_mask:0xf bank_mask:0xf
	v_mov_b32_dpp v83, v111 row_ror:1 row_mask:0xf bank_mask:0xf
	v_mov_b32_dpp v114, v112 row_shr:2 row_mask:0xf bank_mask:0xf
	v_mov_b32_dpp v115, v113 row_shr:2 row_mask:0xf bank_mask:0xf
	v_pk_fma_f32 v[80:81], v[126:127], v[94:95], v[80:81]
	v_mov_b32_dpp v82, v112 row_shr:1 row_mask:0xf bank_mask:0xf
	v_mov_b32_dpp v83, v113 row_shr:1 row_mask:0xf bank_mask:0xf
	v_pk_fma_f32 v[114:115], v[96:97], v[114:115], v[98:99]
	v_mul_f32_e32 v79, 0xbfb8aa3b, v80
	v_pk_fma_f32 v[82:83], v[100:101], v[82:83], v[114:115]
	v_cvt_f32_i32_e32 v115, v5
	v_cvt_f32_i32_e32 v114, v29
	v_exp_f32_e32 v79, v79
	s_nop 0
	s_nop 0
	s_nop 0
	s_nop 0
	v_mov_b32_dpp v110, v86 row_ror:1 row_mask:0xf bank_mask:0xf
	v_mov_b32_dpp v124, v86 row_ror:2 row_mask:0xf bank_mask:0xf
	v_mov_b32_dpp v111, v87 row_ror:1 row_mask:0xf bank_mask:0xf
	v_mov_b32_dpp v125, v87 row_ror:2 row_mask:0xf bank_mask:0xf
	v_pk_mul_f32 v[86:87], v[168:169], v[114:115]
	v_add_f32_e32 v79, 1.0, v79
	v_pk_fma_f32 v[108:109], v[84:85], v[104:105], v[108:109]
	v_mov_b32_dpp v124, v86 row_shr:2 row_mask:0xf bank_mask:0xf
	v_mov_b32_dpp v125, v87 row_shr:2 row_mask:0xf bank_mask:0xf
	v_mov_b32_dpp v110, v86 row_shr:1 row_mask:0xf bank_mask:0xf
	v_mov_b32_dpp v111, v87 row_shr:1 row_mask:0xf bank_mask:0xf
	v_pk_fma_f32 v[114:115], v[122:123], v[124:125], v[76:77]
	v_rcp_f32_e32 v79, v79
	v_pk_fma_f32 v[110:111], v[118:119], v[110:111], v[114:115]
	v_mul_f32_e32 v114, 0xbfb8aa3b, v108
	v_exp_f32_e32 v114, v114
	v_pk_fma_f32 v[82:83], v[112:113], v[102:103], v[82:83]
	v_mul_f32_e32 v79, v80, v79
	v_pk_fma_f32 v[110:111], v[86:87], v[106:107], v[110:111]
	v_mul_f32_e32 v79, v79, v81
	v_mul_f32_e32 v81, 0xbfb8aa3b, v82
	v_add_f32_e32 v80, 1.0, v114
	v_exp_f32_e32 v81, v81
	v_mul_f32_e32 v114, 0xbfb8aa3b, v110
	v_rcp_f32_e32 v80, v80
	v_exp_f32_e32 v114, v114
	v_add_f32_e32 v81, 1.0, v81
	v_rcp_f32_e32 v81, v81
	v_mul_f32_e32 v80, v108, v80
	v_add_f32_e32 v108, 1.0, v114
	v_rcp_f32_e32 v108, v108
	v_mul_f32_e32 v81, v82, v81
	v_mul_f32_e32 v80, v80, v109
	v_mul_f32_e32 v81, v81, v83
	v_mul_f32_e32 v82, v110, v108
	v_mul_f32_e32 v82, v82, v111
	v_cvt_pk_bf16_f32 v80, v79, v80
	v_cvt_pk_bf16_f32 v81, v81, v82
	v_mov_b32_e32 v175, v174
	global_store_dwordx2 v[128:129], v[80:81], off offset:8
	s_nop 0
	s_nop 0
	s_nop 0
	s_nop 0
	v_mov_b32_dpp v80, v126 row_ror:1 row_mask:0xf bank_mask:0xf
	v_mov_b32_dpp v82, v126 row_ror:2 row_mask:0xf bank_mask:0xf
	v_mov_b32_dpp v81, v127 row_ror:1 row_mask:0xf bank_mask:0xf
	v_mov_b32_dpp v83, v127 row_ror:2 row_mask:0xf bank_mask:0xf
	v_pk_mul_f32 v[126:127], v[174:175], v[182:183]
	s_nop 0
	s_nop 0
	v_mov_b32_dpp v82, v126 row_shr:2 row_mask:0xf bank_mask:0xf
	v_mov_b32_dpp v83, v127 row_shr:2 row_mask:0xf bank_mask:0xf
	v_mov_b32_dpp v80, v126 row_shr:1 row_mask:0xf bank_mask:0xf
	v_mov_b32_dpp v81, v127 row_shr:1 row_mask:0xf bank_mask:0xf
	v_pk_fma_f32 v[82:83], v[88:89], v[82:83], v[90:91]
	s_nop 0
	v_pk_fma_f32 v[80:81], v[92:93], v[80:81], v[82:83]
	v_mov_b32_dpp v110, v84 row_ror:2 row_mask:0xf bank_mask:0xf
	v_pk_fma_f32 v[80:81], v[126:127], v[94:95], v[80:81]
	s_nop 0
	v_mov_b32_dpp v111, v85 row_ror:2 row_mask:0xf bank_mask:0xf
	v_pk_mul_f32 v[82:83], v[174:175], v[178:179]
	v_mov_b32_dpp v108, v84 row_ror:1 row_mask:0xf bank_mask:0xf
	v_mov_b32_dpp v109, v85 row_ror:1 row_mask:0xf bank_mask:0xf
	v_mov_b32_dpp v110, v82 row_shr:2 row_mask:0xf bank_mask:0xf
	v_mov_b32_dpp v111, v83 row_shr:2 row_mask:0xf bank_mask:0xf
	v_mul_f32_e32 v79, 0xbfb8aa3b, v80
	v_mov_b32_dpp v108, v82 row_shr:1 row_mask:0xf bank_mask:0xf
	v_mov_b32_dpp v109, v83 row_shr:1 row_mask:0xf bank_mask:0xf
	v_pk_fma_f32 v[110:111], v[120:121], v[110:111], v[74:75]
	v_exp_f32_e32 v79, v79
	s_nop 0
	v_pk_fma_f32 v[108:109], v[116:117], v[108:109], v[110:111]
	s_nop 0
	s_nop 0
	v_mov_b32_dpp v114, v112 row_ror:2 row_mask:0xf bank_mask:0xf
	v_pk_fma_f32 v[82:83], v[82:83], v[104:105], v[108:109]
	s_nop 0
	v_mov_b32_dpp v115, v113 row_ror:2 row_mask:0xf bank_mask:0xf
	v_pk_mul_f32 v[108:109], v[174:175], v[180:181]
	v_mov_b32_dpp v84, v112 row_ror:1 row_mask:0xf bank_mask:0xf
	v_mov_b32_dpp v85, v113 row_ror:1 row_mask:0xf bank_mask:0xf
	v_mov_b32_dpp v114, v108 row_shr:2 row_mask:0xf bank_mask:0xf
	v_mov_b32_dpp v115, v109 row_shr:2 row_mask:0xf bank_mask:0xf
	s_nop 0
	s_nop 0
	v_mov_b32_dpp v84, v108 row_shr:1 row_mask:0xf bank_mask:0xf
	v_mov_b32_dpp v85, v109 row_shr:1 row_mask:0xf bank_mask:0xf
	v_pk_fma_f32 v[110:111], v[96:97], v[114:115], v[98:99]
	s_nop 0
	s_nop 0
	v_add_f32_e32 v79, 1.0, v79
	v_mov_b32_dpp v112, v86 row_ror:1 row_mask:0xf bank_mask:0xf
	v_mov_b32_dpp v124, v86 row_ror:2 row_mask:0xf bank_mask:0xf
	v_pk_fma_f32 v[84:85], v[100:101], v[84:85], v[110:111]
	v_mov_b32_dpp v113, v87 row_ror:1 row_mask:0xf bank_mask:0xf
	v_mov_b32_dpp v125, v87 row_ror:2 row_mask:0xf bank_mask:0xf
	v_pk_mul_f32 v[86:87], v[174:175], v[176:177]
	v_rcp_f32_e32 v79, v79
	v_mul_f32_e32 v110, 0xbfb8aa3b, v82
	v_mov_b32_dpp v124, v86 row_shr:2 row_mask:0xf bank_mask:0xf
	v_mov_b32_dpp v125, v87 row_shr:2 row_mask:0xf bank_mask:0xf
	v_exp_f32_e32 v110, v110
	v_pk_fma_f32 v[84:85], v[108:109], v[102:103], v[84:85]
	v_mov_b32_dpp v112, v86 row_shr:1 row_mask:0xf bank_mask:0xf
	v_mov_b32_dpp v113, v87 row_shr:1 row_mask:0xf bank_mask:0xf
	v_pk_fma_f32 v[108:109], v[122:123], v[124:125], v[76:77]
	v_mul_f32_e32 v79, v80, v79
	v_pk_fma_f32 v[108:109], v[118:119], v[112:113], v[108:109]
	v_mul_f32_e32 v79, v79, v81
	v_pk_fma_f32 v[86:87], v[86:87], v[106:107], v[108:109]
	v_add_f32_e32 v80, 1.0, v110
	v_mul_f32_e32 v81, 0xbfb8aa3b, v84
	v_mul_f32_e32 v108, 0xbfb8aa3b, v86
	v_rcp_f32_e32 v80, v80
	v_exp_f32_e32 v81, v81
	v_exp_f32_e32 v108, v108
	v_mov_b32_e32 v78, 0
	v_mul_f32_e32 v80, v82, v80
	v_add_f32_e32 v81, 1.0, v81
	v_add_f32_e32 v82, 1.0, v108
	v_rcp_f32_e32 v81, v81
	v_rcp_f32_e32 v82, v82
	v_mul_f32_e32 v80, v80, v83
	v_cvt_pk_bf16_f32 v80, v79, v80
	v_mul_f32_e32 v81, v84, v81
	v_mul_f32_e32 v82, v86, v82
	v_mul_f32_e32 v81, v81, v85
	v_mul_f32_e32 v82, v82, v87
	v_cvt_pk_bf16_f32 v81, v81, v82
	v_mov_b32_e32 v82, 0
	v_mov_b32_e32 v83, 0
	v_mov_b32_e32 v84, 0
	v_mov_b32_e32 v85, 0
	global_store_dwordx2 v[132:133], v[80:81], off offset:8
	s_and_saveexec_b64 s[0:1], vcc
	ds_read_b128 v[82:85], v195 offset:16
	s_or_b64 exec, exec, s[0:1]
	v_mov_b32_e32 v79, 0
	v_mov_b32_e32 v80, 0
	v_mov_b32_e32 v81, 0
	s_and_saveexec_b64 s[0:1], vcc
	ds_read_b128 v[78:81], v195 offset:528
	s_or_b64 exec, exec, s[0:1]
	v_cvt_f32_i32_e32 v127, v66
	v_cvt_f32_i32_e32 v67, v67
	v_cvt_f32_i32_e32 v66, v71
	v_cvt_f32_i32_e32 v126, v70
	v_mov_b32_e32 v86, v157
	v_mov_b32_e32 v108, v157
	v_mov_b32_e32 v209, v208
	s_waitcnt lgkmcnt(0)
	v_mov_b32_dpp v86, v82 row_ror:1 row_mask:0xf bank_mask:0xf
	v_mov_b32_dpp v108, v82 row_ror:2 row_mask:0xf bank_mask:0xf
	v_mov_b32_e32 v82, v157
	v_mov_b32_e32 v110, v157
	v_mov_b32_e32 v111, v157
	v_mov_b32_dpp v82, v83 row_ror:1 row_mask:0xf bank_mask:0xf
	v_mov_b32_dpp v110, v83 row_ror:2 row_mask:0xf bank_mask:0xf
	v_mov_b32_e32 v87, v157
	v_mov_b32_e32 v109, v157
	v_mov_b32_e32 v83, v157
	v_mov_b32_dpp v111, v79 row_ror:2 row_mask:0xf bank_mask:0xf
	v_pk_mul_f32 v[66:67], v[208:209], v[66:67]
	v_mov_b32_dpp v87, v78 row_ror:1 row_mask:0xf bank_mask:0xf
	v_mov_b32_dpp v109, v78 row_ror:2 row_mask:0xf bank_mask:0xf
	v_pk_mul_f32 v[126:127], v[208:209], v[126:127]
	v_mov_b32_dpp v83, v79 row_ror:1 row_mask:0xf bank_mask:0xf
	v_mov_b32_dpp v110, v66 row_shr:2 row_mask:0xf bank_mask:0xf
	v_mov_b32_dpp v111, v67 row_shr:2 row_mask:0xf bank_mask:0xf
	v_cvt_f32_i32_e32 v79, v68
	v_cvt_f32_i32_e32 v78, v72
	v_cvt_f32_i32_e32 v69, v69
	v_cvt_f32_i32_e32 v68, v73
	v_mov_b32_e32 v112, v157
	v_mov_b32_e32 v114, v157
	v_mov_b32_dpp v108, v126 row_shr:2 row_mask:0xf bank_mask:0xf
	v_mov_b32_dpp v109, v127 row_shr:2 row_mask:0xf bank_mask:0xf
	v_mov_b32_dpp v82, v66 row_shr:1 row_mask:0xf bank_mask:0xf
	v_mov_b32_dpp v83, v67 row_shr:1 row_mask:0xf bank_mask:0xf
	v_pk_fma_f32 v[70:71], v[120:121], v[110:111], v[74:75]
	v_mov_b32_dpp v112, v84 row_ror:1 row_mask:0xf bank_mask:0xf
	v_mov_b32_dpp v114, v84 row_ror:2 row_mask:0xf bank_mask:0xf
	v_mov_b32_e32 v84, v157
	v_mov_b32_e32 v124, v157
	v_mov_b32_dpp v86, v126 row_shr:1 row_mask:0xf bank_mask:0xf
	v_mov_b32_dpp v87, v127 row_shr:1 row_mask:0xf bank_mask:0xf
	v_pk_fma_f32 v[108:109], v[88:89], v[108:109], v[90:91]
	v_pk_fma_f32 v[70:71], v[116:117], v[82:83], v[70:71]
	v_mov_b32_dpp v84, v85 row_ror:1 row_mask:0xf bank_mask:0xf
	v_mov_b32_dpp v124, v85 row_ror:2 row_mask:0xf bank_mask:0xf
	v_pk_fma_f32 v[86:87], v[92:93], v[86:87], v[108:109]
	v_pk_fma_f32 v[70:71], v[66:67], v[104:105], v[70:71]
	v_mov_b32_e32 v115, v157
	v_mov_b32_e32 v85, v157
	v_mov_b32_e32 v125, v157
	v_pk_fma_f32 v[86:87], v[126:127], v[94:95], v[86:87]
	v_mov_b32_e32 v113, v157
	v_mov_b32_dpp v115, v80 row_ror:2 row_mask:0xf bank_mask:0xf
	v_pk_mul_f32 v[78:79], v[208:209], v[78:79]
	v_mov_b32_dpp v85, v81 row_ror:1 row_mask:0xf bank_mask:0xf
	v_mov_b32_dpp v125, v81 row_ror:2 row_mask:0xf bank_mask:0xf
	v_pk_mul_f32 v[68:69], v[208:209], v[68:69]
	v_mul_f32_e32 v81, 0xbfb8aa3b, v70
	v_mov_b32_dpp v113, v80 row_ror:1 row_mask:0xf bank_mask:0xf
	v_mov_b32_dpp v114, v78 row_shr:2 row_mask:0xf bank_mask:0xf
	v_mov_b32_dpp v115, v79 row_shr:2 row_mask:0xf bank_mask:0xf
	v_mov_b32_dpp v124, v68 row_shr:2 row_mask:0xf bank_mask:0xf
	v_mul_f32_e32 v72, 0xbfb8aa3b, v86
	v_mov_b32_dpp v125, v69 row_shr:2 row_mask:0xf bank_mask:0xf
	v_exp_f32_e32 v81, v81
	v_mov_b32_dpp v112, v78 row_shr:1 row_mask:0xf bank_mask:0xf
	v_mov_b32_dpp v113, v79 row_shr:1 row_mask:0xf bank_mask:0xf
	v_pk_fma_f32 v[82:83], v[96:97], v[114:115], v[98:99]
	v_mov_b32_dpp v84, v68 row_shr:1 row_mask:0xf bank_mask:0xf
	v_mov_b32_dpp v85, v69 row_shr:1 row_mask:0xf bank_mask:0xf
	v_exp_f32_e32 v80, v72
	v_pk_fma_f32 v[72:73], v[122:123], v[124:125], v[76:77]
	v_pk_fma_f32 v[82:83], v[100:101], v[112:113], v[82:83]
	v_pk_fma_f32 v[72:73], v[118:119], v[84:85], v[72:73]
	v_pk_fma_f32 v[82:83], v[78:79], v[102:103], v[82:83]
	v_pk_fma_f32 v[72:73], v[68:69], v[106:107], v[72:73]
	v_add_f32_e32 v81, 1.0, v81
	v_mul_f32_e32 v84, 0xbfb8aa3b, v82
	v_mul_f32_e32 v85, 0xbfb8aa3b, v72
	v_rcp_f32_e32 v81, v81
	v_exp_f32_e32 v84, v84
	v_exp_f32_e32 v85, v85
	v_add_f32_e32 v80, 1.0, v80
	v_mul_f32_e32 v70, v70, v81
	v_add_f32_e32 v81, 1.0, v84
	v_add_f32_e32 v84, 1.0, v85
	v_rcp_f32_e32 v81, v81
	v_rcp_f32_e32 v84, v84
	v_rcp_f32_e32 v80, v80
	v_cvt_f32_i32_e32 v109, v58
	v_cvt_f32_i32_e32 v108, v62
	v_mul_f32_e32 v70, v70, v71
	v_mul_f32_e32 v71, v82, v81
	v_mul_f32_e32 v72, v72, v84
	v_mul_f32_e32 v80, v86, v80
	v_mul_f32_e32 v71, v71, v83
	v_mul_f32_e32 v72, v72, v73
	v_mov_b32_e32 v207, v206
	v_mul_f32_e32 v80, v80, v87
	v_cvt_pk_bf16_f32 v70, v80, v70
	v_cvt_pk_bf16_f32 v71, v71, v72
	v_mov_b32_e32 v72, v157
	v_mov_b32_e32 v73, v157
	global_store_dwordx2 v[130:131], v[70:71], off offset:8
	v_mov_b32_e32 v70, v157
	v_mov_b32_dpp v72, v126 row_ror:2 row_mask:0xf bank_mask:0xf
	v_mov_b32_e32 v71, v157
	v_mov_b32_dpp v73, v127 row_ror:2 row_mask:0xf bank_mask:0xf
	v_pk_mul_f32 v[108:109], v[206:207], v[108:109]
	v_mov_b32_dpp v70, v126 row_ror:1 row_mask:0xf bank_mask:0xf
	v_mov_b32_dpp v71, v127 row_ror:1 row_mask:0xf bank_mask:0xf
	v_mov_b32_dpp v72, v108 row_shr:2 row_mask:0xf bank_mask:0xf
	v_mov_b32_dpp v73, v109 row_shr:2 row_mask:0xf bank_mask:0xf
	v_mov_b32_dpp v70, v108 row_shr:1 row_mask:0xf bank_mask:0xf
	v_mov_b32_dpp v71, v109 row_shr:1 row_mask:0xf bank_mask:0xf
	v_pk_fma_f32 v[72:73], v[88:89], v[72:73], v[90:91]
	v_cvt_f32_i32_e32 v59, v59
	v_cvt_f32_i32_e32 v58, v63
	v_mov_b32_e32 v80, v157
	v_mov_b32_e32 v82, v157
	v_pk_fma_f32 v[70:71], v[92:93], v[70:71], v[72:73]
	v_mov_b32_dpp v80, v66 row_ror:1 row_mask:0xf bank_mask:0xf
	v_mov_b32_dpp v82, v66 row_ror:2 row_mask:0xf bank_mask:0xf
	v_mov_b32_e32 v66, v157
	v_mov_b32_e32 v84, v157
	v_pk_fma_f32 v[70:71], v[108:109], v[94:95], v[70:71]
	v_mov_b32_dpp v66, v78 row_ror:1 row_mask:0xf bank_mask:0xf
	v_mov_b32_dpp v84, v78 row_ror:2 row_mask:0xf bank_mask:0xf
	v_mov_b32_e32 v78, v157
	v_mov_b32_e32 v86, v157
	v_mov_b32_e32 v83, v157
	v_cvt_f32_i32_e32 v72, v64
	v_mul_f32_e32 v64, 0xbfb8aa3b, v70
	v_mov_b32_dpp v78, v68 row_ror:1 row_mask:0xf bank_mask:0xf
	v_mov_b32_dpp v86, v68 row_ror:2 row_mask:0xf bank_mask:0xf
	v_mov_b32_e32 v81, v157
	v_mov_b32_dpp v83, v67 row_ror:2 row_mask:0xf bank_mask:0xf
	v_pk_mul_f32 v[58:59], v[206:207], v[58:59]
	v_exp_f32_e32 v68, v64
	v_mov_b32_dpp v81, v67 row_ror:1 row_mask:0xf bank_mask:0xf
	v_mov_b32_dpp v82, v58 row_shr:2 row_mask:0xf bank_mask:0xf
	v_mov_b32_dpp v83, v59 row_shr:2 row_mask:0xf bank_mask:0xf
	v_cvt_f32_i32_e32 v73, v60
	v_cvt_f32_i32_e32 v61, v61
	v_cvt_f32_i32_e32 v60, v65
	v_mov_b32_dpp v80, v58 row_shr:1 row_mask:0xf bank_mask:0xf
	v_mov_b32_dpp v81, v59 row_shr:1 row_mask:0xf bank_mask:0xf
	v_pk_fma_f32 v[62:63], v[120:121], v[82:83], v[74:75]
	v_mov_b32_e32 v67, v157
	v_pk_fma_f32 v[62:63], v[116:117], v[80:81], v[62:63]
	v_mov_b32_e32 v85, v157
	v_pk_fma_f32 v[62:63], v[58:59], v[104:105], v[62:63]
	v_mov_b32_dpp v67, v79 row_ror:1 row_mask:0xf bank_mask:0xf
	v_mov_b32_dpp v85, v79 row_ror:2 row_mask:0xf bank_mask:0xf
	v_mov_b32_e32 v79, v157
	v_mov_b32_e32 v87, v157
	v_add_f32_e32 v68, 1.0, v68
	v_pk_mul_f32 v[72:73], v[206:207], v[72:73]
	v_mov_b32_dpp v79, v69 row_ror:1 row_mask:0xf bank_mask:0xf
	v_mov_b32_dpp v87, v69 row_ror:2 row_mask:0xf bank_mask:0xf
	v_pk_mul_f32 v[60:61], v[206:207], v[60:61]
	v_rcp_f32_e32 v68, v68
	v_mul_f32_e32 v69, 0xbfb8aa3b, v62
	v_mov_b32_dpp v84, v72 row_shr:2 row_mask:0xf bank_mask:0xf
	v_mov_b32_dpp v85, v73 row_shr:2 row_mask:0xf bank_mask:0xf
	v_mov_b32_dpp v86, v60 row_shr:2 row_mask:0xf bank_mask:0xf
	v_mov_b32_dpp v87, v61 row_shr:2 row_mask:0xf bank_mask:0xf
	v_exp_f32_e32 v69, v69
	v_mov_b32_dpp v66, v72 row_shr:1 row_mask:0xf bank_mask:0xf
	v_mov_b32_dpp v67, v73 row_shr:1 row_mask:0xf bank_mask:0xf
	v_pk_fma_f32 v[80:81], v[96:97], v[84:85], v[98:99]
	v_mov_b32_dpp v78, v60 row_shr:1 row_mask:0xf bank_mask:0xf
	v_mov_b32_dpp v79, v61 row_shr:1 row_mask:0xf bank_mask:0xf
	v_pk_fma_f32 v[64:65], v[122:123], v[86:87], v[76:77]
	v_pk_fma_f32 v[66:67], v[100:101], v[66:67], v[80:81]
	v_pk_fma_f32 v[64:65], v[118:119], v[78:79], v[64:65]
	v_pk_fma_f32 v[66:67], v[72:73], v[102:103], v[66:67]
	v_pk_fma_f32 v[64:65], v[60:61], v[106:107], v[64:65]
	v_mul_f32_e32 v68, v70, v68
	v_mul_f32_e32 v68, v68, v71
	v_add_f32_e32 v69, 1.0, v69
	v_mul_f32_e32 v70, 0xbfb8aa3b, v66
	v_mul_f32_e32 v71, 0xbfb8aa3b, v64
	v_rcp_f32_e32 v69, v69
	v_exp_f32_e32 v70, v70
	v_exp_f32_e32 v71, v71
	v_cvt_f32_i32_e32 v81, v50
	v_mul_f32_e32 v62, v62, v69
	v_add_f32_e32 v69, 1.0, v70
	v_add_f32_e32 v70, 1.0, v71
	v_rcp_f32_e32 v69, v69
	v_rcp_f32_e32 v70, v70
	v_cvt_f32_i32_e32 v80, v54
	v_mul_f32_e32 v62, v62, v63
	v_mul_f32_e32 v63, v66, v69
	v_mul_f32_e32 v64, v64, v70
	v_mul_f32_e32 v63, v63, v67
	v_mul_f32_e32 v64, v64, v65
	v_mov_b32_e32 v199, v198
	v_cvt_pk_bf16_f32 v62, v68, v62
	v_cvt_pk_bf16_f32 v63, v63, v64
	v_mov_b32_e32 v64, v157
	v_mov_b32_e32 v65, v157
	global_store_dwordx2 v[134:135], v[62:63], off offset:8
	v_mov_b32_e32 v62, v157
	v_mov_b32_dpp v64, v108 row_ror:2 row_mask:0xf bank_mask:0xf
	v_mov_b32_e32 v63, v157
	v_mov_b32_dpp v65, v109 row_ror:2 row_mask:0xf bank_mask:0xf
	v_pk_mul_f32 v[80:81], v[198:199], v[80:81]
	v_mov_b32_dpp v62, v108 row_ror:1 row_mask:0xf bank_mask:0xf
	v_mov_b32_dpp v63, v109 row_ror:1 row_mask:0xf bank_mask:0xf
	v_mov_b32_dpp v64, v80 row_shr:2 row_mask:0xf bank_mask:0xf
	v_mov_b32_dpp v65, v81 row_shr:2 row_mask:0xf bank_mask:0xf
	v_mov_b32_dpp v62, v80 row_shr:1 row_mask:0xf bank_mask:0xf
	v_mov_b32_dpp v63, v81 row_shr:1 row_mask:0xf bank_mask:0xf
	v_pk_fma_f32 v[64:65], v[88:89], v[64:65], v[90:91]
	v_cvt_f32_i32_e32 v51, v51
	v_cvt_f32_i32_e32 v50, v55
	v_mov_b32_e32 v66, v157
	v_mov_b32_e32 v68, v157
	v_pk_fma_f32 v[62:63], v[92:93], v[62:63], v[64:65]
	v_mov_b32_dpp v66, v58 row_ror:1 row_mask:0xf bank_mask:0xf
	v_mov_b32_dpp v68, v58 row_ror:2 row_mask:0xf bank_mask:0xf
	v_mov_b32_e32 v58, v157
	v_mov_b32_e32 v70, v157
	v_pk_fma_f32 v[62:63], v[80:81], v[94:95], v[62:63]
	v_mov_b32_dpp v58, v72 row_ror:1 row_mask:0xf bank_mask:0xf
	v_mov_b32_dpp v70, v72 row_ror:2 row_mask:0xf bank_mask:0xf
	v_mov_b32_e32 v72, v157
	v_mov_b32_e32 v78, v157
	v_mov_b32_e32 v69, v157
	v_cvt_f32_i32_e32 v64, v56
	v_mul_f32_e32 v56, 0xbfb8aa3b, v62
	v_mov_b32_dpp v72, v60 row_ror:1 row_mask:0xf bank_mask:0xf
	v_mov_b32_dpp v78, v60 row_ror:2 row_mask:0xf bank_mask:0xf
	v_mov_b32_e32 v67, v157
	v_mov_b32_dpp v69, v59 row_ror:2 row_mask:0xf bank_mask:0xf
	v_pk_mul_f32 v[50:51], v[198:199], v[50:51]
	v_exp_f32_e32 v60, v56
	v_mov_b32_dpp v67, v59 row_ror:1 row_mask:0xf bank_mask:0xf
	v_mov_b32_dpp v68, v50 row_shr:2 row_mask:0xf bank_mask:0xf
	v_mov_b32_dpp v69, v51 row_shr:2 row_mask:0xf bank_mask:0xf
	v_cvt_f32_i32_e32 v65, v52
	v_cvt_f32_i32_e32 v53, v53
	v_cvt_f32_i32_e32 v52, v57
	v_mov_b32_dpp v66, v50 row_shr:1 row_mask:0xf bank_mask:0xf
	v_mov_b32_dpp v67, v51 row_shr:1 row_mask:0xf bank_mask:0xf
	v_pk_fma_f32 v[54:55], v[120:121], v[68:69], v[74:75]
	v_mov_b32_e32 v59, v157
	v_pk_fma_f32 v[54:55], v[116:117], v[66:67], v[54:55]
	v_mov_b32_e32 v71, v157
	v_pk_fma_f32 v[54:55], v[50:51], v[104:105], v[54:55]
	v_mov_b32_dpp v59, v73 row_ror:1 row_mask:0xf bank_mask:0xf
	v_mov_b32_dpp v71, v73 row_ror:2 row_mask:0xf bank_mask:0xf
	v_mov_b32_e32 v73, v157
	v_mov_b32_e32 v79, v157
	v_add_f32_e32 v60, 1.0, v60
	v_pk_mul_f32 v[64:65], v[198:199], v[64:65]
	v_mov_b32_dpp v73, v61 row_ror:1 row_mask:0xf bank_mask:0xf
	v_mov_b32_dpp v79, v61 row_ror:2 row_mask:0xf bank_mask:0xf
	v_pk_mul_f32 v[52:53], v[198:199], v[52:53]
	v_rcp_f32_e32 v60, v60
	v_mul_f32_e32 v61, 0xbfb8aa3b, v54
	v_mov_b32_dpp v70, v64 row_shr:2 row_mask:0xf bank_mask:0xf
	v_mov_b32_dpp v71, v65 row_shr:2 row_mask:0xf bank_mask:0xf
	v_mov_b32_dpp v78, v52 row_shr:2 row_mask:0xf bank_mask:0xf
	v_mov_b32_dpp v79, v53 row_shr:2 row_mask:0xf bank_mask:0xf
	v_exp_f32_e32 v61, v61
	v_mov_b32_dpp v58, v64 row_shr:1 row_mask:0xf bank_mask:0xf
	v_mov_b32_dpp v59, v65 row_shr:1 row_mask:0xf bank_mask:0xf
	v_pk_fma_f32 v[66:67], v[96:97], v[70:71], v[98:99]
	v_mov_b32_dpp v72, v52 row_shr:1 row_mask:0xf bank_mask:0xf
	v_mov_b32_dpp v73, v53 row_shr:1 row_mask:0xf bank_mask:0xf
	v_pk_fma_f32 v[56:57], v[122:123], v[78:79], v[76:77]
	v_pk_fma_f32 v[58:59], v[100:101], v[58:59], v[66:67]
	v_pk_fma_f32 v[56:57], v[118:119], v[72:73], v[56:57]
	v_pk_fma_f32 v[58:59], v[64:65], v[102:103], v[58:59]
	v_pk_fma_f32 v[56:57], v[52:53], v[106:107], v[56:57]
	v_mul_f32_e32 v60, v62, v60
	v_mul_f32_e32 v60, v60, v63
	v_add_f32_e32 v61, 1.0, v61
	v_mul_f32_e32 v62, 0xbfb8aa3b, v58
	v_mul_f32_e32 v63, 0xbfb8aa3b, v56
	v_rcp_f32_e32 v61, v61
	v_exp_f32_e32 v62, v62
	v_exp_f32_e32 v63, v63
	v_mov_b32_e32 v195, v194
	v_mul_f32_e32 v54, v54, v61
	v_add_f32_e32 v61, 1.0, v62
	v_add_f32_e32 v62, 1.0, v63
	v_rcp_f32_e32 v61, v61
	v_rcp_f32_e32 v62, v62
	v_mul_f32_e32 v54, v54, v55
	v_cvt_pk_bf16_f32 v54, v60, v54
	v_mul_f32_e32 v55, v58, v61
	v_mul_f32_e32 v56, v56, v62
	v_mul_f32_e32 v55, v55, v59
	v_mul_f32_e32 v56, v56, v57
	v_cvt_pk_bf16_f32 v55, v55, v56
	v_mov_b32_e32 v56, v157
	v_mov_b32_e32 v57, v157
	global_store_dwordx2 v[136:137], v[54:55], off offset:8
	v_mov_b32_e32 v54, v157
	v_mov_b32_dpp v56, v80 row_ror:2 row_mask:0xf bank_mask:0xf
	v_mov_b32_e32 v55, v157
	v_mov_b32_dpp v57, v81 row_ror:2 row_mask:0xf bank_mask:0xf
	v_pk_mul_f32 v[68:69], v[194:195], v[204:205]
	v_mov_b32_dpp v54, v80 row_ror:1 row_mask:0xf bank_mask:0xf
	v_mov_b32_dpp v55, v81 row_ror:1 row_mask:0xf bank_mask:0xf
	v_mov_b32_dpp v56, v68 row_shr:2 row_mask:0xf bank_mask:0xf
	v_mov_b32_dpp v57, v69 row_shr:2 row_mask:0xf bank_mask:0xf
	v_mov_b32_e32 v60, v157
	v_mov_b32_dpp v54, v68 row_shr:1 row_mask:0xf bank_mask:0xf
	v_mov_b32_dpp v55, v69 row_shr:1 row_mask:0xf bank_mask:0xf
	v_pk_fma_f32 v[56:57], v[88:89], v[56:57], v[90:91]
	v_mov_b32_e32 v61, v157
	v_mov_b32_e32 v58, v157
	v_mov_b32_dpp v60, v50 row_ror:2 row_mask:0xf bank_mask:0xf
	v_pk_fma_f32 v[54:55], v[92:93], v[54:55], v[56:57]
	v_mov_b32_e32 v59, v157
	v_mov_b32_dpp v61, v51 row_ror:2 row_mask:0xf bank_mask:0xf
	v_pk_mul_f32 v[56:57], v[194:195], v[202:203]
	v_mov_b32_dpp v58, v50 row_ror:1 row_mask:0xf bank_mask:0xf
	v_mov_b32_dpp v59, v51 row_ror:1 row_mask:0xf bank_mask:0xf
	v_mov_b32_dpp v60, v56 row_shr:2 row_mask:0xf bank_mask:0xf
	v_mov_b32_dpp v61, v57 row_shr:2 row_mask:0xf bank_mask:0xf
	v_mov_b32_dpp v58, v56 row_shr:1 row_mask:0xf bank_mask:0xf
	v_mov_b32_dpp v59, v57 row_shr:1 row_mask:0xf bank_mask:0xf
	v_pk_fma_f32 v[60:61], v[120:121], v[60:61], v[74:75]
	v_mov_b32_e32 v62, v157
	v_pk_fma_f32 v[58:59], v[116:117], v[58:59], v[60:61]
	v_mov_b32_e32 v63, v157
	v_mov_b32_e32 v50, v157
	v_mov_b32_dpp v62, v64 row_ror:2 row_mask:0xf bank_mask:0xf
	v_pk_fma_f32 v[56:57], v[56:57], v[104:105], v[58:59]
	v_mov_b32_e32 v51, v157
	v_mov_b32_dpp v63, v65 row_ror:2 row_mask:0xf bank_mask:0xf
	v_pk_mul_f32 v[58:59], v[194:195], v[200:201]
	v_mov_b32_dpp v50, v64 row_ror:1 row_mask:0xf bank_mask:0xf
	v_mov_b32_dpp v51, v65 row_ror:1 row_mask:0xf bank_mask:0xf
	v_mov_b32_dpp v62, v58 row_shr:2 row_mask:0xf bank_mask:0xf
	v_mov_b32_dpp v63, v59 row_shr:2 row_mask:0xf bank_mask:0xf
	v_mov_b32_dpp v50, v58 row_shr:1 row_mask:0xf bank_mask:0xf
	v_mov_b32_dpp v51, v59 row_shr:1 row_mask:0xf bank_mask:0xf
	v_pk_fma_f32 v[60:61], v[96:97], v[62:63], v[98:99]
	v_pk_fma_f32 v[54:55], v[68:69], v[94:95], v[54:55]
	v_pk_fma_f32 v[50:51], v[100:101], v[50:51], v[60:61]
	v_mov_b32_e32 v64, v157
	v_pk_fma_f32 v[50:51], v[58:59], v[102:103], v[50:51]
	v_mul_f32_e32 v58, 0xbfb8aa3b, v54
	v_exp_f32_e32 v60, v58
	v_mov_b32_e32 v66, v157
	v_mov_b32_e32 v65, v157
	v_mov_b32_e32 v67, v157
	v_add_f32_e32 v60, 1.0, v60
	v_rcp_f32_e32 v60, v60
	v_mul_f32_e32 v61, 0xbfb8aa3b, v56
	v_mov_b32_dpp v64, v52 row_ror:1 row_mask:0xf bank_mask:0xf
	v_mov_b32_dpp v66, v52 row_ror:2 row_mask:0xf bank_mask:0xf
	v_mov_b32_dpp v65, v53 row_ror:1 row_mask:0xf bank_mask:0xf
	v_mov_b32_dpp v67, v53 row_ror:2 row_mask:0xf bank_mask:0xf
	v_pk_mul_f32 v[52:53], v[194:195], v[196:197]
	v_exp_f32_e32 v61, v61
	v_mul_f32_e32 v54, v54, v60
	v_mov_b32_dpp v66, v52 row_shr:2 row_mask:0xf bank_mask:0xf
	v_mov_b32_dpp v67, v53 row_shr:2 row_mask:0xf bank_mask:0xf
	v_mov_b32_dpp v64, v52 row_shr:1 row_mask:0xf bank_mask:0xf
	v_mov_b32_dpp v65, v53 row_shr:1 row_mask:0xf bank_mask:0xf
	v_pk_fma_f32 v[58:59], v[122:123], v[66:67], v[76:77]
	v_mul_f32_e32 v54, v54, v55
	v_pk_fma_f32 v[58:59], v[118:119], v[64:65], v[58:59]
	v_add_f32_e32 v55, 1.0, v61
	v_pk_fma_f32 v[52:53], v[52:53], v[106:107], v[58:59]
	v_mul_f32_e32 v58, 0xbfb8aa3b, v50
	v_rcp_f32_e32 v55, v55
	v_exp_f32_e32 v58, v58
	v_mul_f32_e32 v59, 0xbfb8aa3b, v52
	v_exp_f32_e32 v59, v59
	v_mul_f32_e32 v55, v56, v55
	v_add_f32_e32 v56, 1.0, v58
	v_rcp_f32_e32 v56, v56
	v_add_f32_e32 v58, 1.0, v59
	v_rcp_f32_e32 v58, v58
	v_mul_f32_e32 v50, v50, v56
	v_mul_f32_e32 v51, v50, v51
	v_mul_f32_e32 v50, v52, v58
	v_mul_f32_e32 v55, v55, v57
	v_mul_f32_e32 v52, v50, v53
	v_cvt_pk_bf16_f32 v50, v54, v55
	v_cvt_pk_bf16_f32 v51, v51, v52
	global_store_dwordx2 v[138:139], v[50:51], off offset:8
